# line-aligned A windows (3-buffer LDS ring) + hand-written loader and compute main loop with per-fragment W1 rotation
# speedup vs baseline: 1.0014x; 1.0014x over previous
.LBB1_247:
	s_or_b64 exec, exec, s[2:3]
	v_mov_b32_e32 v110, v18
	v_mov_b32_e32 v111, v19
	v_mov_b32_e32 v112, v20
	v_mov_b32_e32 v113, v21
	s_mov_b32 s72, 0x2000
	s_mov_b32 s73, 0
	s_mov_b32 s74, 0x20000
	s_mov_b32 s75, 0
	v_lshl_add_u64 v[158:159], v[158:159], 0, s[74:75]
	v_mul_u32_u24_e32 v163, 0x110, v160
	v_lshl_add_u32 v162, v1, 4, v163
	global_load_dwordx4 v[94:97], v[158:159], off
	v_lshl_add_u64 v[158:159], v[158:159], 0, s[72:73]
	global_load_dwordx4 v[98:101], v[158:159], off
	v_lshl_add_u64 v[158:159], v[158:159], 0, s[72:73]
	global_load_dwordx4 v[102:105], v[158:159], off
	v_lshl_add_u64 v[158:159], v[158:159], 0, s[72:73]
	global_load_dwordx4 v[106:109], v[158:159], off
	v_lshl_add_u64 v[158:159], v[158:159], 0, s[72:73]
	global_load_dwordx4 v[142:145], v[158:159], off
	v_lshl_add_u64 v[158:159], v[158:159], 0, s[72:73]
	global_load_dwordx4 v[146:149], v[158:159], off
	v_lshl_add_u64 v[158:159], v[158:159], 0, s[72:73]
	global_load_dwordx4 v[150:153], v[158:159], off
	v_lshl_add_u64 v[158:159], v[158:159], 0, s[72:73]
	global_load_dwordx4 v[154:157], v[158:159], off
	v_lshl_add_u64 v[158:159], v[158:159], 0, s[72:73]
	s_waitcnt lgkmcnt(0)
	s_barrier
	ds_read_b128 v[114:117], v162 offset:0
	ds_read_b128 v[118:121], v162 offset:8704
	ds_read_b128 v[122:125], v162 offset:32
	ds_read_b128 v[126:129], v162 offset:8736
	ds_read_b128 v[130:133], v162 offset:64
	ds_read_b128 v[134:137], v162 offset:8768
	s_waitcnt lgkmcnt(5)
	v_mfma_f32_32x32x16_f16 v[2:17], v[114:117], v[110:113], 0
	s_waitcnt lgkmcnt(4)
	v_mfma_f32_32x32x16_f16 v[18:33], v[118:121], v[110:113], 0
	ds_read_b128 v[114:117], v162 offset:96
	ds_read_b128 v[118:121], v162 offset:8800
	global_load_dwordx4 v[110:113], v[158:159], off
	v_lshl_add_u64 v[158:159], v[158:159], 0, s[72:73]
	s_waitcnt lgkmcnt(5)
	v_mfma_f32_32x32x16_f16 v[2:17], v[122:125], v[90:93], v[2:17]
	s_waitcnt lgkmcnt(4)
	v_mfma_f32_32x32x16_f16 v[18:33], v[126:129], v[90:93], v[18:33]
	ds_read_b128 v[122:125], v162 offset:128
	ds_read_b128 v[126:129], v162 offset:8832
	global_load_dwordx4 v[90:93], v[158:159], off
	v_lshl_add_u64 v[158:159], v[158:159], 0, s[72:73]
	s_waitcnt lgkmcnt(5)
	v_mfma_f32_32x32x16_f16 v[2:17], v[130:133], v[86:89], v[2:17]
	s_waitcnt lgkmcnt(4)
	v_mfma_f32_32x32x16_f16 v[18:33], v[134:137], v[86:89], v[18:33]
	ds_read_b128 v[130:133], v162 offset:160
	ds_read_b128 v[134:137], v162 offset:8864
	global_load_dwordx4 v[86:89], v[158:159], off
	v_lshl_add_u64 v[158:159], v[158:159], 0, s[72:73]
	s_waitcnt lgkmcnt(5)
	v_mfma_f32_32x32x16_f16 v[2:17], v[114:117], v[82:85], v[2:17]
	s_waitcnt lgkmcnt(4)
	v_mfma_f32_32x32x16_f16 v[18:33], v[118:121], v[82:85], v[18:33]
	ds_read_b128 v[114:117], v162 offset:192
	ds_read_b128 v[118:121], v162 offset:8896
	global_load_dwordx4 v[82:85], v[158:159], off
	v_lshl_add_u64 v[158:159], v[158:159], 0, s[72:73]
	s_waitcnt lgkmcnt(5)
	v_mfma_f32_32x32x16_f16 v[2:17], v[122:125], v[78:81], v[2:17]
	s_waitcnt lgkmcnt(4)
	v_mfma_f32_32x32x16_f16 v[18:33], v[126:129], v[78:81], v[18:33]
	ds_read_b128 v[122:125], v162 offset:224
	ds_read_b128 v[126:129], v162 offset:8928
	global_load_dwordx4 v[78:81], v[158:159], off
	v_lshl_add_u64 v[158:159], v[158:159], 0, s[72:73]
	s_waitcnt lgkmcnt(5)
	v_mfma_f32_32x32x16_f16 v[2:17], v[130:133], v[74:77], v[2:17]
	s_waitcnt lgkmcnt(4)
	v_mfma_f32_32x32x16_f16 v[18:33], v[134:137], v[74:77], v[18:33]
	global_load_dwordx4 v[74:77], v[158:159], off
	v_lshl_add_u64 v[158:159], v[158:159], 0, s[72:73]
	s_waitcnt lgkmcnt(3)
	v_mfma_f32_32x32x16_f16 v[2:17], v[114:117], v[70:73], v[2:17]
	s_waitcnt lgkmcnt(2)
	v_mfma_f32_32x32x16_f16 v[18:33], v[118:121], v[70:73], v[18:33]
	global_load_dwordx4 v[70:73], v[158:159], off
	v_lshl_add_u64 v[158:159], v[158:159], 0, s[72:73]
	s_waitcnt lgkmcnt(1)
	v_mfma_f32_32x32x16_f16 v[2:17], v[122:125], v[66:69], v[2:17]
	s_waitcnt lgkmcnt(0)
	v_mfma_f32_32x32x16_f16 v[18:33], v[126:129], v[66:69], v[18:33]
	global_load_dwordx4 v[66:69], v[158:159], off
	v_lshl_add_u64 v[158:159], v[158:159], 0, s[72:73]
	s_waitcnt lgkmcnt(0)
	s_barrier
	ds_read_b128 v[114:117], v162 offset:17408
	ds_read_b128 v[118:121], v162 offset:26112
	ds_read_b128 v[122:125], v162 offset:17440
	ds_read_b128 v[126:129], v162 offset:26144
	ds_read_b128 v[130:133], v162 offset:17472
	ds_read_b128 v[134:137], v162 offset:26176
	s_waitcnt lgkmcnt(5)
	v_mfma_f32_32x32x16_f16 v[2:17], v[114:117], v[62:65], v[2:17]
	s_waitcnt lgkmcnt(4)
	v_mfma_f32_32x32x16_f16 v[18:33], v[118:121], v[62:65], v[18:33]
	ds_read_b128 v[114:117], v162 offset:17504
	ds_read_b128 v[118:121], v162 offset:26208
	global_load_dwordx4 v[62:65], v[158:159], off
	v_lshl_add_u64 v[158:159], v[158:159], 0, s[72:73]
	s_waitcnt lgkmcnt(5)
	v_mfma_f32_32x32x16_f16 v[2:17], v[122:125], v[58:61], v[2:17]
	s_waitcnt lgkmcnt(4)
	v_mfma_f32_32x32x16_f16 v[18:33], v[126:129], v[58:61], v[18:33]
	ds_read_b128 v[122:125], v162 offset:17536
	ds_read_b128 v[126:129], v162 offset:26240
	global_load_dwordx4 v[58:61], v[158:159], off
	v_lshl_add_u64 v[158:159], v[158:159], 0, s[72:73]
	s_waitcnt lgkmcnt(5)
	v_mfma_f32_32x32x16_f16 v[2:17], v[130:133], v[54:57], v[2:17]
	s_waitcnt lgkmcnt(4)
	v_mfma_f32_32x32x16_f16 v[18:33], v[134:137], v[54:57], v[18:33]
	ds_read_b128 v[130:133], v162 offset:17568
	ds_read_b128 v[134:137], v162 offset:26272
	global_load_dwordx4 v[54:57], v[158:159], off
	v_lshl_add_u64 v[158:159], v[158:159], 0, s[72:73]
	s_waitcnt lgkmcnt(5)
	v_mfma_f32_32x32x16_f16 v[2:17], v[114:117], v[50:53], v[2:17]
	s_waitcnt lgkmcnt(4)
	v_mfma_f32_32x32x16_f16 v[18:33], v[118:121], v[50:53], v[18:33]
	ds_read_b128 v[114:117], v162 offset:17600
	ds_read_b128 v[118:121], v162 offset:26304
	global_load_dwordx4 v[50:53], v[158:159], off
	v_lshl_add_u64 v[158:159], v[158:159], 0, s[72:73]
	s_waitcnt lgkmcnt(5)
	v_mfma_f32_32x32x16_f16 v[2:17], v[122:125], v[46:49], v[2:17]
	s_waitcnt lgkmcnt(4)
	v_mfma_f32_32x32x16_f16 v[18:33], v[126:129], v[46:49], v[18:33]
	ds_read_b128 v[122:125], v162 offset:17632
	ds_read_b128 v[126:129], v162 offset:26336
	global_load_dwordx4 v[46:49], v[158:159], off
	v_lshl_add_u64 v[158:159], v[158:159], 0, s[72:73]
	s_waitcnt lgkmcnt(5)
	v_mfma_f32_32x32x16_f16 v[2:17], v[130:133], v[42:45], v[2:17]
	s_waitcnt lgkmcnt(4)
	v_mfma_f32_32x32x16_f16 v[18:33], v[134:137], v[42:45], v[18:33]
	global_load_dwordx4 v[42:45], v[158:159], off
	v_lshl_add_u64 v[158:159], v[158:159], 0, s[72:73]
	s_waitcnt lgkmcnt(3)
	v_mfma_f32_32x32x16_f16 v[2:17], v[114:117], v[38:41], v[2:17]
	s_waitcnt lgkmcnt(2)
	v_mfma_f32_32x32x16_f16 v[18:33], v[118:121], v[38:41], v[18:33]
	global_load_dwordx4 v[38:41], v[158:159], off
	v_lshl_add_u64 v[158:159], v[158:159], 0, s[72:73]
	s_waitcnt lgkmcnt(1)
	v_mfma_f32_32x32x16_f16 v[2:17], v[122:125], v[34:37], v[2:17]
	s_waitcnt lgkmcnt(0)
	v_mfma_f32_32x32x16_f16 v[18:33], v[126:129], v[34:37], v[18:33]
	global_load_dwordx4 v[34:37], v[158:159], off
	v_lshl_add_u64 v[158:159], v[158:159], 0, s[72:73]
	s_waitcnt lgkmcnt(0)
	s_barrier
	ds_read_b128 v[114:117], v162 offset:34816
	ds_read_b128 v[118:121], v162 offset:43520
	ds_read_b128 v[122:125], v162 offset:34848
	ds_read_b128 v[126:129], v162 offset:43552
	ds_read_b128 v[130:133], v162 offset:34880
	ds_read_b128 v[134:137], v162 offset:43584
	s_waitcnt vmcnt(23)
	s_waitcnt lgkmcnt(5)
	v_mfma_f32_32x32x16_f16 v[2:17], v[114:117], v[94:97], v[2:17]
	s_waitcnt lgkmcnt(4)
	v_mfma_f32_32x32x16_f16 v[18:33], v[118:121], v[94:97], v[18:33]
	ds_read_b128 v[114:117], v162 offset:34912
	ds_read_b128 v[118:121], v162 offset:43616
	global_load_dwordx4 v[94:97], v[158:159], off
	v_lshl_add_u64 v[158:159], v[158:159], 0, s[72:73]
	s_waitcnt vmcnt(23)
	s_waitcnt lgkmcnt(5)
	v_mfma_f32_32x32x16_f16 v[2:17], v[122:125], v[98:101], v[2:17]
	s_waitcnt lgkmcnt(4)
	v_mfma_f32_32x32x16_f16 v[18:33], v[126:129], v[98:101], v[18:33]
	ds_read_b128 v[122:125], v162 offset:34944
	ds_read_b128 v[126:129], v162 offset:43648
	global_load_dwordx4 v[98:101], v[158:159], off
	v_lshl_add_u64 v[158:159], v[158:159], 0, s[72:73]
	s_waitcnt vmcnt(23)
	s_waitcnt lgkmcnt(5)
	v_mfma_f32_32x32x16_f16 v[2:17], v[130:133], v[102:105], v[2:17]
	s_waitcnt lgkmcnt(4)
	v_mfma_f32_32x32x16_f16 v[18:33], v[134:137], v[102:105], v[18:33]
	ds_read_b128 v[130:133], v162 offset:34976
	ds_read_b128 v[134:137], v162 offset:43680
	global_load_dwordx4 v[102:105], v[158:159], off
	v_lshl_add_u64 v[158:159], v[158:159], 0, s[72:73]
	s_waitcnt vmcnt(23)
	s_waitcnt lgkmcnt(5)
	v_mfma_f32_32x32x16_f16 v[2:17], v[114:117], v[106:109], v[2:17]
	s_waitcnt lgkmcnt(4)
	v_mfma_f32_32x32x16_f16 v[18:33], v[118:121], v[106:109], v[18:33]
	ds_read_b128 v[114:117], v162 offset:35008
	ds_read_b128 v[118:121], v162 offset:43712
	global_load_dwordx4 v[106:109], v[158:159], off
	v_lshl_add_u64 v[158:159], v[158:159], 0, s[72:73]
	s_waitcnt vmcnt(23)
	s_waitcnt lgkmcnt(5)
	v_mfma_f32_32x32x16_f16 v[2:17], v[122:125], v[142:145], v[2:17]
	s_waitcnt lgkmcnt(4)
	v_mfma_f32_32x32x16_f16 v[18:33], v[126:129], v[142:145], v[18:33]
	ds_read_b128 v[122:125], v162 offset:35040
	ds_read_b128 v[126:129], v162 offset:43744
	global_load_dwordx4 v[142:145], v[158:159], off
	v_lshl_add_u64 v[158:159], v[158:159], 0, s[72:73]
	s_waitcnt vmcnt(23)
	s_waitcnt lgkmcnt(5)
	v_mfma_f32_32x32x16_f16 v[2:17], v[130:133], v[146:149], v[2:17]
	s_waitcnt lgkmcnt(4)
	v_mfma_f32_32x32x16_f16 v[18:33], v[134:137], v[146:149], v[18:33]
	global_load_dwordx4 v[146:149], v[158:159], off
	v_lshl_add_u64 v[158:159], v[158:159], 0, s[72:73]
	s_waitcnt vmcnt(23)
	s_waitcnt lgkmcnt(3)
	v_mfma_f32_32x32x16_f16 v[2:17], v[114:117], v[150:153], v[2:17]
	s_waitcnt lgkmcnt(2)
	v_mfma_f32_32x32x16_f16 v[18:33], v[118:121], v[150:153], v[18:33]
	global_load_dwordx4 v[150:153], v[158:159], off
	v_lshl_add_u64 v[158:159], v[158:159], 0, s[72:73]
	s_waitcnt vmcnt(23)
	s_waitcnt lgkmcnt(1)
	v_mfma_f32_32x32x16_f16 v[2:17], v[122:125], v[154:157], v[2:17]
	s_waitcnt lgkmcnt(0)
	v_mfma_f32_32x32x16_f16 v[18:33], v[126:129], v[154:157], v[18:33]
	global_load_dwordx4 v[154:157], v[158:159], off
	v_lshl_add_u64 v[158:159], v[158:159], 0, s[72:73]
	s_waitcnt lgkmcnt(0)
	s_barrier
	ds_read_b128 v[114:117], v162 offset:0
	ds_read_b128 v[118:121], v162 offset:8704
	ds_read_b128 v[122:125], v162 offset:32
	ds_read_b128 v[126:129], v162 offset:8736
	ds_read_b128 v[130:133], v162 offset:64
	ds_read_b128 v[134:137], v162 offset:8768
	s_waitcnt vmcnt(23)
	s_waitcnt lgkmcnt(5)
	v_mfma_f32_32x32x16_f16 v[2:17], v[114:117], v[110:113], v[2:17]
	s_waitcnt lgkmcnt(4)
	v_mfma_f32_32x32x16_f16 v[18:33], v[118:121], v[110:113], v[18:33]
	ds_read_b128 v[114:117], v162 offset:96
	ds_read_b128 v[118:121], v162 offset:8800
	global_load_dwordx4 v[110:113], v[158:159], off
	v_lshl_add_u64 v[158:159], v[158:159], 0, s[72:73]
	s_waitcnt vmcnt(23)
	s_waitcnt lgkmcnt(5)
	v_mfma_f32_32x32x16_f16 v[2:17], v[122:125], v[90:93], v[2:17]
	s_waitcnt lgkmcnt(4)
	v_mfma_f32_32x32x16_f16 v[18:33], v[126:129], v[90:93], v[18:33]
	ds_read_b128 v[122:125], v162 offset:128
	ds_read_b128 v[126:129], v162 offset:8832
	global_load_dwordx4 v[90:93], v[158:159], off
	v_lshl_add_u64 v[158:159], v[158:159], 0, s[72:73]
	s_waitcnt vmcnt(23)
	s_waitcnt lgkmcnt(5)
	v_mfma_f32_32x32x16_f16 v[2:17], v[130:133], v[86:89], v[2:17]
	s_waitcnt lgkmcnt(4)
	v_mfma_f32_32x32x16_f16 v[18:33], v[134:137], v[86:89], v[18:33]
	ds_read_b128 v[130:133], v162 offset:160
	ds_read_b128 v[134:137], v162 offset:8864
	global_load_dwordx4 v[86:89], v[158:159], off
	v_lshl_add_u64 v[158:159], v[158:159], 0, s[72:73]
	s_waitcnt vmcnt(23)
	s_waitcnt lgkmcnt(5)
	v_mfma_f32_32x32x16_f16 v[2:17], v[114:117], v[82:85], v[2:17]
	s_waitcnt lgkmcnt(4)
	v_mfma_f32_32x32x16_f16 v[18:33], v[118:121], v[82:85], v[18:33]
	ds_read_b128 v[114:117], v162 offset:192
	ds_read_b128 v[118:121], v162 offset:8896
	global_load_dwordx4 v[82:85], v[158:159], off
	v_lshl_add_u64 v[158:159], v[158:159], 0, s[72:73]
	s_waitcnt vmcnt(23)
	s_waitcnt lgkmcnt(5)
	v_mfma_f32_32x32x16_f16 v[2:17], v[122:125], v[78:81], v[2:17]
	s_waitcnt lgkmcnt(4)
	v_mfma_f32_32x32x16_f16 v[18:33], v[126:129], v[78:81], v[18:33]
	ds_read_b128 v[122:125], v162 offset:224
	ds_read_b128 v[126:129], v162 offset:8928
	global_load_dwordx4 v[78:81], v[158:159], off
	v_lshl_add_u64 v[158:159], v[158:159], 0, s[72:73]
	s_waitcnt vmcnt(23)
	s_waitcnt lgkmcnt(5)
	v_mfma_f32_32x32x16_f16 v[2:17], v[130:133], v[74:77], v[2:17]
	s_waitcnt lgkmcnt(4)
	v_mfma_f32_32x32x16_f16 v[18:33], v[134:137], v[74:77], v[18:33]
	global_load_dwordx4 v[74:77], v[158:159], off
	v_lshl_add_u64 v[158:159], v[158:159], 0, s[72:73]
	s_waitcnt vmcnt(23)
	s_waitcnt lgkmcnt(3)
	v_mfma_f32_32x32x16_f16 v[2:17], v[114:117], v[70:73], v[2:17]
	s_waitcnt lgkmcnt(2)
	v_mfma_f32_32x32x16_f16 v[18:33], v[118:121], v[70:73], v[18:33]
	global_load_dwordx4 v[70:73], v[158:159], off
	v_lshl_add_u64 v[158:159], v[158:159], 0, s[72:73]
	s_waitcnt vmcnt(23)
	s_waitcnt lgkmcnt(1)
	v_mfma_f32_32x32x16_f16 v[2:17], v[122:125], v[66:69], v[2:17]
	s_waitcnt lgkmcnt(0)
	v_mfma_f32_32x32x16_f16 v[18:33], v[126:129], v[66:69], v[18:33]
	global_load_dwordx4 v[66:69], v[158:159], off
	v_lshl_add_u64 v[158:159], v[158:159], 0, s[72:73]
	s_waitcnt lgkmcnt(0)
	s_barrier
	ds_read_b128 v[114:117], v162 offset:17408
	ds_read_b128 v[118:121], v162 offset:26112
	ds_read_b128 v[122:125], v162 offset:17440
	ds_read_b128 v[126:129], v162 offset:26144
	ds_read_b128 v[130:133], v162 offset:17472
	ds_read_b128 v[134:137], v162 offset:26176
	s_waitcnt vmcnt(23)
	s_waitcnt lgkmcnt(5)
	v_mfma_f32_32x32x16_f16 v[2:17], v[114:117], v[62:65], v[2:17]
	s_waitcnt lgkmcnt(4)
	v_mfma_f32_32x32x16_f16 v[18:33], v[118:121], v[62:65], v[18:33]
	ds_read_b128 v[114:117], v162 offset:17504
	ds_read_b128 v[118:121], v162 offset:26208
	global_load_dwordx4 v[62:65], v[158:159], off
	v_lshl_add_u64 v[158:159], v[158:159], 0, s[72:73]
	s_waitcnt vmcnt(23)
	s_waitcnt lgkmcnt(5)
	v_mfma_f32_32x32x16_f16 v[2:17], v[122:125], v[58:61], v[2:17]
	s_waitcnt lgkmcnt(4)
	v_mfma_f32_32x32x16_f16 v[18:33], v[126:129], v[58:61], v[18:33]
	ds_read_b128 v[122:125], v162 offset:17536
	ds_read_b128 v[126:129], v162 offset:26240
	global_load_dwordx4 v[58:61], v[158:159], off
	v_lshl_add_u64 v[158:159], v[158:159], 0, s[72:73]
	s_waitcnt vmcnt(23)
	s_waitcnt lgkmcnt(5)
	v_mfma_f32_32x32x16_f16 v[2:17], v[130:133], v[54:57], v[2:17]
	s_waitcnt lgkmcnt(4)
	v_mfma_f32_32x32x16_f16 v[18:33], v[134:137], v[54:57], v[18:33]
	ds_read_b128 v[130:133], v162 offset:17568
	ds_read_b128 v[134:137], v162 offset:26272
	global_load_dwordx4 v[54:57], v[158:159], off
	v_lshl_add_u64 v[158:159], v[158:159], 0, s[72:73]
	s_waitcnt vmcnt(23)
	s_waitcnt lgkmcnt(5)
	v_mfma_f32_32x32x16_f16 v[2:17], v[114:117], v[50:53], v[2:17]
	s_waitcnt lgkmcnt(4)
	v_mfma_f32_32x32x16_f16 v[18:33], v[118:121], v[50:53], v[18:33]
	ds_read_b128 v[114:117], v162 offset:17600
	ds_read_b128 v[118:121], v162 offset:26304
	global_load_dwordx4 v[50:53], v[158:159], off
	v_lshl_add_u64 v[158:159], v[158:159], 0, s[72:73]
	s_waitcnt vmcnt(23)
	s_waitcnt lgkmcnt(5)
	v_mfma_f32_32x32x16_f16 v[2:17], v[122:125], v[46:49], v[2:17]
	s_waitcnt lgkmcnt(4)
	v_mfma_f32_32x32x16_f16 v[18:33], v[126:129], v[46:49], v[18:33]
	ds_read_b128 v[122:125], v162 offset:17632
	ds_read_b128 v[126:129], v162 offset:26336
	global_load_dwordx4 v[46:49], v[158:159], off
	v_lshl_add_u64 v[158:159], v[158:159], 0, s[72:73]
	s_waitcnt vmcnt(23)
	s_waitcnt lgkmcnt(5)
	v_mfma_f32_32x32x16_f16 v[2:17], v[130:133], v[42:45], v[2:17]
	s_waitcnt lgkmcnt(4)
	v_mfma_f32_32x32x16_f16 v[18:33], v[134:137], v[42:45], v[18:33]
	global_load_dwordx4 v[42:45], v[158:159], off
	v_lshl_add_u64 v[158:159], v[158:159], 0, s[72:73]
	s_waitcnt vmcnt(23)
	s_waitcnt lgkmcnt(3)
	v_mfma_f32_32x32x16_f16 v[2:17], v[114:117], v[38:41], v[2:17]
	s_waitcnt lgkmcnt(2)
	v_mfma_f32_32x32x16_f16 v[18:33], v[118:121], v[38:41], v[18:33]
	global_load_dwordx4 v[38:41], v[158:159], off
	v_lshl_add_u64 v[158:159], v[158:159], 0, s[72:73]
	s_waitcnt vmcnt(23)
	s_waitcnt lgkmcnt(1)
	v_mfma_f32_32x32x16_f16 v[2:17], v[122:125], v[34:37], v[2:17]
	s_waitcnt lgkmcnt(0)
	v_mfma_f32_32x32x16_f16 v[18:33], v[126:129], v[34:37], v[18:33]
	global_load_dwordx4 v[34:37], v[158:159], off
	v_lshl_add_u64 v[158:159], v[158:159], 0, s[72:73]
	s_waitcnt lgkmcnt(0)
	s_barrier
	ds_read_b128 v[114:117], v162 offset:34816
	ds_read_b128 v[118:121], v162 offset:43520
	ds_read_b128 v[122:125], v162 offset:34848
	ds_read_b128 v[126:129], v162 offset:43552
	ds_read_b128 v[130:133], v162 offset:34880
	ds_read_b128 v[134:137], v162 offset:43584
	s_waitcnt vmcnt(23)
	s_waitcnt lgkmcnt(5)
	v_mfma_f32_32x32x16_f16 v[2:17], v[114:117], v[94:97], v[2:17]
	s_waitcnt lgkmcnt(4)
	v_mfma_f32_32x32x16_f16 v[18:33], v[118:121], v[94:97], v[18:33]
	ds_read_b128 v[114:117], v162 offset:34912
	ds_read_b128 v[118:121], v162 offset:43616
	global_load_dwordx4 v[94:97], v[158:159], off
	v_lshl_add_u64 v[158:159], v[158:159], 0, s[72:73]
	s_waitcnt vmcnt(23)
	s_waitcnt lgkmcnt(5)
	v_mfma_f32_32x32x16_f16 v[2:17], v[122:125], v[98:101], v[2:17]
	s_waitcnt lgkmcnt(4)
	v_mfma_f32_32x32x16_f16 v[18:33], v[126:129], v[98:101], v[18:33]
	ds_read_b128 v[122:125], v162 offset:34944
	ds_read_b128 v[126:129], v162 offset:43648
	global_load_dwordx4 v[98:101], v[158:159], off
	v_lshl_add_u64 v[158:159], v[158:159], 0, s[72:73]
	s_waitcnt vmcnt(23)
	s_waitcnt lgkmcnt(5)
	v_mfma_f32_32x32x16_f16 v[2:17], v[130:133], v[102:105], v[2:17]
	s_waitcnt lgkmcnt(4)
	v_mfma_f32_32x32x16_f16 v[18:33], v[134:137], v[102:105], v[18:33]
	ds_read_b128 v[130:133], v162 offset:34976
	ds_read_b128 v[134:137], v162 offset:43680
	global_load_dwordx4 v[102:105], v[158:159], off
	v_lshl_add_u64 v[158:159], v[158:159], 0, s[72:73]
	s_waitcnt vmcnt(23)
	s_waitcnt lgkmcnt(5)
	v_mfma_f32_32x32x16_f16 v[2:17], v[114:117], v[106:109], v[2:17]
	s_waitcnt lgkmcnt(4)
	v_mfma_f32_32x32x16_f16 v[18:33], v[118:121], v[106:109], v[18:33]
	ds_read_b128 v[114:117], v162 offset:35008
	ds_read_b128 v[118:121], v162 offset:43712
	global_load_dwordx4 v[106:109], v[158:159], off
	v_lshl_add_u64 v[158:159], v[158:159], 0, s[72:73]
	s_waitcnt vmcnt(23)
	s_waitcnt lgkmcnt(5)
	v_mfma_f32_32x32x16_f16 v[2:17], v[122:125], v[142:145], v[2:17]
	s_waitcnt lgkmcnt(4)
	v_mfma_f32_32x32x16_f16 v[18:33], v[126:129], v[142:145], v[18:33]
	ds_read_b128 v[122:125], v162 offset:35040
	ds_read_b128 v[126:129], v162 offset:43744
	global_load_dwordx4 v[142:145], v[158:159], off
	v_lshl_add_u64 v[158:159], v[158:159], 0, s[72:73]
	s_waitcnt vmcnt(23)
	s_waitcnt lgkmcnt(5)
	v_mfma_f32_32x32x16_f16 v[2:17], v[130:133], v[146:149], v[2:17]
	s_waitcnt lgkmcnt(4)
	v_mfma_f32_32x32x16_f16 v[18:33], v[134:137], v[146:149], v[18:33]
	global_load_dwordx4 v[146:149], v[158:159], off
	v_lshl_add_u64 v[158:159], v[158:159], 0, s[72:73]
	s_waitcnt vmcnt(23)
	s_waitcnt lgkmcnt(3)
	v_mfma_f32_32x32x16_f16 v[2:17], v[114:117], v[150:153], v[2:17]
	s_waitcnt lgkmcnt(2)
	v_mfma_f32_32x32x16_f16 v[18:33], v[118:121], v[150:153], v[18:33]
	global_load_dwordx4 v[150:153], v[158:159], off
	v_lshl_add_u64 v[158:159], v[158:159], 0, s[72:73]
	s_waitcnt vmcnt(23)
	s_waitcnt lgkmcnt(1)
	v_mfma_f32_32x32x16_f16 v[2:17], v[122:125], v[154:157], v[2:17]
	s_waitcnt lgkmcnt(0)
	v_mfma_f32_32x32x16_f16 v[18:33], v[126:129], v[154:157], v[18:33]
	global_load_dwordx4 v[154:157], v[158:159], off
	v_lshl_add_u64 v[158:159], v[158:159], 0, s[72:73]
	s_waitcnt lgkmcnt(0)
	s_barrier
	ds_read_b128 v[114:117], v162 offset:0
	ds_read_b128 v[118:121], v162 offset:8704
	ds_read_b128 v[122:125], v162 offset:32
	ds_read_b128 v[126:129], v162 offset:8736
	ds_read_b128 v[130:133], v162 offset:64
	ds_read_b128 v[134:137], v162 offset:8768
	s_waitcnt vmcnt(23)
	s_waitcnt lgkmcnt(5)
	v_mfma_f32_32x32x16_f16 v[2:17], v[114:117], v[110:113], v[2:17]
	s_waitcnt lgkmcnt(4)
	v_mfma_f32_32x32x16_f16 v[18:33], v[118:121], v[110:113], v[18:33]
	ds_read_b128 v[114:117], v162 offset:96
	ds_read_b128 v[118:121], v162 offset:8800
	global_load_dwordx4 v[110:113], v[158:159], off
	v_lshl_add_u64 v[158:159], v[158:159], 0, s[72:73]
	s_waitcnt vmcnt(23)
	s_waitcnt lgkmcnt(5)
	v_mfma_f32_32x32x16_f16 v[2:17], v[122:125], v[90:93], v[2:17]
	s_waitcnt lgkmcnt(4)
	v_mfma_f32_32x32x16_f16 v[18:33], v[126:129], v[90:93], v[18:33]
	ds_read_b128 v[122:125], v162 offset:128
	ds_read_b128 v[126:129], v162 offset:8832
	global_load_dwordx4 v[90:93], v[158:159], off
	v_lshl_add_u64 v[158:159], v[158:159], 0, s[72:73]
	s_waitcnt vmcnt(23)
	s_waitcnt lgkmcnt(5)
	v_mfma_f32_32x32x16_f16 v[2:17], v[130:133], v[86:89], v[2:17]
	s_waitcnt lgkmcnt(4)
	v_mfma_f32_32x32x16_f16 v[18:33], v[134:137], v[86:89], v[18:33]
	ds_read_b128 v[130:133], v162 offset:160
	ds_read_b128 v[134:137], v162 offset:8864
	global_load_dwordx4 v[86:89], v[158:159], off
	v_lshl_add_u64 v[158:159], v[158:159], 0, s[72:73]
	s_waitcnt vmcnt(23)
	s_waitcnt lgkmcnt(5)
	v_mfma_f32_32x32x16_f16 v[2:17], v[114:117], v[82:85], v[2:17]
	s_waitcnt lgkmcnt(4)
	v_mfma_f32_32x32x16_f16 v[18:33], v[118:121], v[82:85], v[18:33]
	ds_read_b128 v[114:117], v162 offset:192
	ds_read_b128 v[118:121], v162 offset:8896
	global_load_dwordx4 v[82:85], v[158:159], off
	v_lshl_add_u64 v[158:159], v[158:159], 0, s[72:73]
	s_waitcnt vmcnt(23)
	s_waitcnt lgkmcnt(5)
	v_mfma_f32_32x32x16_f16 v[2:17], v[122:125], v[78:81], v[2:17]
	s_waitcnt lgkmcnt(4)
	v_mfma_f32_32x32x16_f16 v[18:33], v[126:129], v[78:81], v[18:33]
	ds_read_b128 v[122:125], v162 offset:224
	ds_read_b128 v[126:129], v162 offset:8928
	global_load_dwordx4 v[78:81], v[158:159], off
	v_lshl_add_u64 v[158:159], v[158:159], 0, s[72:73]
	s_waitcnt vmcnt(23)
	s_waitcnt lgkmcnt(5)
	v_mfma_f32_32x32x16_f16 v[2:17], v[130:133], v[74:77], v[2:17]
	s_waitcnt lgkmcnt(4)
	v_mfma_f32_32x32x16_f16 v[18:33], v[134:137], v[74:77], v[18:33]
	global_load_dwordx4 v[74:77], v[158:159], off
	v_lshl_add_u64 v[158:159], v[158:159], 0, s[72:73]
	s_waitcnt vmcnt(23)
	s_waitcnt lgkmcnt(3)
	v_mfma_f32_32x32x16_f16 v[2:17], v[114:117], v[70:73], v[2:17]
	s_waitcnt lgkmcnt(2)
	v_mfma_f32_32x32x16_f16 v[18:33], v[118:121], v[70:73], v[18:33]
	global_load_dwordx4 v[70:73], v[158:159], off
	v_lshl_add_u64 v[158:159], v[158:159], 0, s[72:73]
	s_waitcnt vmcnt(23)
	s_waitcnt lgkmcnt(1)
	v_mfma_f32_32x32x16_f16 v[2:17], v[122:125], v[66:69], v[2:17]
	s_waitcnt lgkmcnt(0)
	v_mfma_f32_32x32x16_f16 v[18:33], v[126:129], v[66:69], v[18:33]
	global_load_dwordx4 v[66:69], v[158:159], off
	v_lshl_add_u64 v[158:159], v[158:159], 0, s[72:73]
	s_waitcnt lgkmcnt(0)
	s_barrier
	ds_read_b128 v[114:117], v162 offset:17408
	ds_read_b128 v[118:121], v162 offset:26112
	ds_read_b128 v[122:125], v162 offset:17440
	ds_read_b128 v[126:129], v162 offset:26144
	ds_read_b128 v[130:133], v162 offset:17472
	ds_read_b128 v[134:137], v162 offset:26176
	s_waitcnt vmcnt(23)
	s_waitcnt lgkmcnt(5)
	v_mfma_f32_32x32x16_f16 v[2:17], v[114:117], v[62:65], v[2:17]
	s_waitcnt lgkmcnt(4)
	v_mfma_f32_32x32x16_f16 v[18:33], v[118:121], v[62:65], v[18:33]
	ds_read_b128 v[114:117], v162 offset:17504
	ds_read_b128 v[118:121], v162 offset:26208
	global_load_dwordx4 v[62:65], v[158:159], off
	v_lshl_add_u64 v[158:159], v[158:159], 0, s[72:73]
	s_waitcnt vmcnt(23)
	s_waitcnt lgkmcnt(5)
	v_mfma_f32_32x32x16_f16 v[2:17], v[122:125], v[58:61], v[2:17]
	s_waitcnt lgkmcnt(4)
	v_mfma_f32_32x32x16_f16 v[18:33], v[126:129], v[58:61], v[18:33]
	ds_read_b128 v[122:125], v162 offset:17536
	ds_read_b128 v[126:129], v162 offset:26240
	global_load_dwordx4 v[58:61], v[158:159], off
	v_lshl_add_u64 v[158:159], v[158:159], 0, s[72:73]
	s_waitcnt vmcnt(23)
	s_waitcnt lgkmcnt(5)
	v_mfma_f32_32x32x16_f16 v[2:17], v[130:133], v[54:57], v[2:17]
	s_waitcnt lgkmcnt(4)
	v_mfma_f32_32x32x16_f16 v[18:33], v[134:137], v[54:57], v[18:33]
	ds_read_b128 v[130:133], v162 offset:17568
	ds_read_b128 v[134:137], v162 offset:26272
	global_load_dwordx4 v[54:57], v[158:159], off
	v_lshl_add_u64 v[158:159], v[158:159], 0, s[72:73]
	s_waitcnt vmcnt(23)
	s_waitcnt lgkmcnt(5)
	v_mfma_f32_32x32x16_f16 v[2:17], v[114:117], v[50:53], v[2:17]
	s_waitcnt lgkmcnt(4)
	v_mfma_f32_32x32x16_f16 v[18:33], v[118:121], v[50:53], v[18:33]
	ds_read_b128 v[114:117], v162 offset:17600
	ds_read_b128 v[118:121], v162 offset:26304
	global_load_dwordx4 v[50:53], v[158:159], off
	v_lshl_add_u64 v[158:159], v[158:159], 0, s[72:73]
	s_waitcnt vmcnt(23)
	s_waitcnt lgkmcnt(5)
	v_mfma_f32_32x32x16_f16 v[2:17], v[122:125], v[46:49], v[2:17]
	s_waitcnt lgkmcnt(4)
	v_mfma_f32_32x32x16_f16 v[18:33], v[126:129], v[46:49], v[18:33]
	ds_read_b128 v[122:125], v162 offset:17632
	ds_read_b128 v[126:129], v162 offset:26336
	global_load_dwordx4 v[46:49], v[158:159], off
	v_lshl_add_u64 v[158:159], v[158:159], 0, s[72:73]
	s_waitcnt vmcnt(23)
	s_waitcnt lgkmcnt(5)
	v_mfma_f32_32x32x16_f16 v[2:17], v[130:133], v[42:45], v[2:17]
	s_waitcnt lgkmcnt(4)
	v_mfma_f32_32x32x16_f16 v[18:33], v[134:137], v[42:45], v[18:33]
	global_load_dwordx4 v[42:45], v[158:159], off
	v_lshl_add_u64 v[158:159], v[158:159], 0, s[72:73]
	s_waitcnt vmcnt(23)
	s_waitcnt lgkmcnt(3)
	v_mfma_f32_32x32x16_f16 v[2:17], v[114:117], v[38:41], v[2:17]
	s_waitcnt lgkmcnt(2)
	v_mfma_f32_32x32x16_f16 v[18:33], v[118:121], v[38:41], v[18:33]
	global_load_dwordx4 v[38:41], v[158:159], off
	v_lshl_add_u64 v[158:159], v[158:159], 0, s[72:73]
	s_waitcnt vmcnt(23)
	s_waitcnt lgkmcnt(1)
	v_mfma_f32_32x32x16_f16 v[2:17], v[122:125], v[34:37], v[2:17]
	s_waitcnt lgkmcnt(0)
	v_mfma_f32_32x32x16_f16 v[18:33], v[126:129], v[34:37], v[18:33]
	global_load_dwordx4 v[34:37], v[158:159], off
	v_lshl_add_u64 v[158:159], v[158:159], 0, s[72:73]
	s_waitcnt lgkmcnt(0)
	s_barrier
	ds_read_b128 v[114:117], v162 offset:34816
	ds_read_b128 v[118:121], v162 offset:43520
	ds_read_b128 v[122:125], v162 offset:34848
	ds_read_b128 v[126:129], v162 offset:43552
	ds_read_b128 v[130:133], v162 offset:34880
	ds_read_b128 v[134:137], v162 offset:43584
	s_waitcnt vmcnt(23)
	s_waitcnt lgkmcnt(5)
	v_mfma_f32_32x32x16_f16 v[2:17], v[114:117], v[94:97], v[2:17]
	s_waitcnt lgkmcnt(4)
	v_mfma_f32_32x32x16_f16 v[18:33], v[118:121], v[94:97], v[18:33]
	ds_read_b128 v[114:117], v162 offset:34912
	ds_read_b128 v[118:121], v162 offset:43616
	global_load_dwordx4 v[94:97], v[158:159], off
	v_lshl_add_u64 v[158:159], v[158:159], 0, s[72:73]
	s_waitcnt vmcnt(23)
	s_waitcnt lgkmcnt(5)
	v_mfma_f32_32x32x16_f16 v[2:17], v[122:125], v[98:101], v[2:17]
	s_waitcnt lgkmcnt(4)
	v_mfma_f32_32x32x16_f16 v[18:33], v[126:129], v[98:101], v[18:33]
	ds_read_b128 v[122:125], v162 offset:34944
	ds_read_b128 v[126:129], v162 offset:43648
	global_load_dwordx4 v[98:101], v[158:159], off
	v_lshl_add_u64 v[158:159], v[158:159], 0, s[72:73]
	s_waitcnt vmcnt(23)
	s_waitcnt lgkmcnt(5)
	v_mfma_f32_32x32x16_f16 v[2:17], v[130:133], v[102:105], v[2:17]
	s_waitcnt lgkmcnt(4)
	v_mfma_f32_32x32x16_f16 v[18:33], v[134:137], v[102:105], v[18:33]
	ds_read_b128 v[130:133], v162 offset:34976
	ds_read_b128 v[134:137], v162 offset:43680
	global_load_dwordx4 v[102:105], v[158:159], off
	v_lshl_add_u64 v[158:159], v[158:159], 0, s[72:73]
	s_waitcnt vmcnt(23)
	s_waitcnt lgkmcnt(5)
	v_mfma_f32_32x32x16_f16 v[2:17], v[114:117], v[106:109], v[2:17]
	s_waitcnt lgkmcnt(4)
	v_mfma_f32_32x32x16_f16 v[18:33], v[118:121], v[106:109], v[18:33]
	ds_read_b128 v[114:117], v162 offset:35008
	ds_read_b128 v[118:121], v162 offset:43712
	global_load_dwordx4 v[106:109], v[158:159], off
	v_lshl_add_u64 v[158:159], v[158:159], 0, s[72:73]
	s_waitcnt vmcnt(23)
	s_waitcnt lgkmcnt(5)
	v_mfma_f32_32x32x16_f16 v[2:17], v[122:125], v[142:145], v[2:17]
	s_waitcnt lgkmcnt(4)
	v_mfma_f32_32x32x16_f16 v[18:33], v[126:129], v[142:145], v[18:33]
	ds_read_b128 v[122:125], v162 offset:35040
	ds_read_b128 v[126:129], v162 offset:43744
	global_load_dwordx4 v[142:145], v[158:159], off
	v_lshl_add_u64 v[158:159], v[158:159], 0, s[72:73]
	s_waitcnt vmcnt(23)
	s_waitcnt lgkmcnt(5)
	v_mfma_f32_32x32x16_f16 v[2:17], v[130:133], v[146:149], v[2:17]
	s_waitcnt lgkmcnt(4)
	v_mfma_f32_32x32x16_f16 v[18:33], v[134:137], v[146:149], v[18:33]
	global_load_dwordx4 v[146:149], v[158:159], off
	v_lshl_add_u64 v[158:159], v[158:159], 0, s[72:73]
	s_waitcnt vmcnt(23)
	s_waitcnt lgkmcnt(3)
	v_mfma_f32_32x32x16_f16 v[2:17], v[114:117], v[150:153], v[2:17]
	s_waitcnt lgkmcnt(2)
	v_mfma_f32_32x32x16_f16 v[18:33], v[118:121], v[150:153], v[18:33]
	global_load_dwordx4 v[150:153], v[158:159], off
	v_lshl_add_u64 v[158:159], v[158:159], 0, s[72:73]
	s_waitcnt vmcnt(23)
	s_waitcnt lgkmcnt(1)
	v_mfma_f32_32x32x16_f16 v[2:17], v[122:125], v[154:157], v[2:17]
	s_waitcnt lgkmcnt(0)
	v_mfma_f32_32x32x16_f16 v[18:33], v[126:129], v[154:157], v[18:33]
	global_load_dwordx4 v[154:157], v[158:159], off
	v_lshl_add_u64 v[158:159], v[158:159], 0, s[72:73]
	s_waitcnt lgkmcnt(0)
	s_barrier
	ds_read_b128 v[114:117], v162 offset:0
	ds_read_b128 v[118:121], v162 offset:8704
	ds_read_b128 v[122:125], v162 offset:32
	ds_read_b128 v[126:129], v162 offset:8736
	ds_read_b128 v[130:133], v162 offset:64
	ds_read_b128 v[134:137], v162 offset:8768
	s_waitcnt vmcnt(23)
	s_waitcnt lgkmcnt(5)
	v_mfma_f32_32x32x16_f16 v[2:17], v[114:117], v[110:113], v[2:17]
	s_waitcnt lgkmcnt(4)
	v_mfma_f32_32x32x16_f16 v[18:33], v[118:121], v[110:113], v[18:33]
	ds_read_b128 v[114:117], v162 offset:96
	ds_read_b128 v[118:121], v162 offset:8800
	global_load_dwordx4 v[110:113], v[158:159], off
	v_lshl_add_u64 v[158:159], v[158:159], 0, s[72:73]
	s_waitcnt vmcnt(23)
	s_waitcnt lgkmcnt(5)
	v_mfma_f32_32x32x16_f16 v[2:17], v[122:125], v[90:93], v[2:17]
	s_waitcnt lgkmcnt(4)
	v_mfma_f32_32x32x16_f16 v[18:33], v[126:129], v[90:93], v[18:33]
	ds_read_b128 v[122:125], v162 offset:128
	ds_read_b128 v[126:129], v162 offset:8832
	global_load_dwordx4 v[90:93], v[158:159], off
	v_lshl_add_u64 v[158:159], v[158:159], 0, s[72:73]
	s_waitcnt vmcnt(23)
	s_waitcnt lgkmcnt(5)
	v_mfma_f32_32x32x16_f16 v[2:17], v[130:133], v[86:89], v[2:17]
	s_waitcnt lgkmcnt(4)
	v_mfma_f32_32x32x16_f16 v[18:33], v[134:137], v[86:89], v[18:33]
	ds_read_b128 v[130:133], v162 offset:160
	ds_read_b128 v[134:137], v162 offset:8864
	global_load_dwordx4 v[86:89], v[158:159], off
	v_lshl_add_u64 v[158:159], v[158:159], 0, s[72:73]
	s_waitcnt vmcnt(23)
	s_waitcnt lgkmcnt(5)
	v_mfma_f32_32x32x16_f16 v[2:17], v[114:117], v[82:85], v[2:17]
	s_waitcnt lgkmcnt(4)
	v_mfma_f32_32x32x16_f16 v[18:33], v[118:121], v[82:85], v[18:33]
	ds_read_b128 v[114:117], v162 offset:192
	ds_read_b128 v[118:121], v162 offset:8896
	global_load_dwordx4 v[82:85], v[158:159], off
	v_lshl_add_u64 v[158:159], v[158:159], 0, s[72:73]
	s_waitcnt vmcnt(23)
	s_waitcnt lgkmcnt(5)
	v_mfma_f32_32x32x16_f16 v[2:17], v[122:125], v[78:81], v[2:17]
	s_waitcnt lgkmcnt(4)
	v_mfma_f32_32x32x16_f16 v[18:33], v[126:129], v[78:81], v[18:33]
	ds_read_b128 v[122:125], v162 offset:224
	ds_read_b128 v[126:129], v162 offset:8928
	global_load_dwordx4 v[78:81], v[158:159], off
	v_lshl_add_u64 v[158:159], v[158:159], 0, s[72:73]
	s_waitcnt vmcnt(23)
	s_waitcnt lgkmcnt(5)
	v_mfma_f32_32x32x16_f16 v[2:17], v[130:133], v[74:77], v[2:17]
	s_waitcnt lgkmcnt(4)
	v_mfma_f32_32x32x16_f16 v[18:33], v[134:137], v[74:77], v[18:33]
	global_load_dwordx4 v[74:77], v[158:159], off
	v_lshl_add_u64 v[158:159], v[158:159], 0, s[72:73]
	s_waitcnt vmcnt(23)
	s_waitcnt lgkmcnt(3)
	v_mfma_f32_32x32x16_f16 v[2:17], v[114:117], v[70:73], v[2:17]
	s_waitcnt lgkmcnt(2)
	v_mfma_f32_32x32x16_f16 v[18:33], v[118:121], v[70:73], v[18:33]
	global_load_dwordx4 v[70:73], v[158:159], off
	v_lshl_add_u64 v[158:159], v[158:159], 0, s[72:73]
	s_waitcnt vmcnt(23)
	s_waitcnt lgkmcnt(1)
	v_mfma_f32_32x32x16_f16 v[2:17], v[122:125], v[66:69], v[2:17]
	s_waitcnt lgkmcnt(0)
	v_mfma_f32_32x32x16_f16 v[18:33], v[126:129], v[66:69], v[18:33]
	global_load_dwordx4 v[66:69], v[158:159], off
	v_lshl_add_u64 v[158:159], v[158:159], 0, s[72:73]
	s_waitcnt lgkmcnt(0)
	s_barrier
	ds_read_b128 v[114:117], v162 offset:17408
	ds_read_b128 v[118:121], v162 offset:26112
	ds_read_b128 v[122:125], v162 offset:17440
	ds_read_b128 v[126:129], v162 offset:26144
	ds_read_b128 v[130:133], v162 offset:17472
	ds_read_b128 v[134:137], v162 offset:26176
	s_waitcnt vmcnt(23)
	s_waitcnt lgkmcnt(5)
	v_mfma_f32_32x32x16_f16 v[2:17], v[114:117], v[62:65], v[2:17]
	s_waitcnt lgkmcnt(4)
	v_mfma_f32_32x32x16_f16 v[18:33], v[118:121], v[62:65], v[18:33]
	ds_read_b128 v[114:117], v162 offset:17504
	ds_read_b128 v[118:121], v162 offset:26208
	global_load_dwordx4 v[62:65], v[158:159], off
	v_lshl_add_u64 v[158:159], v[158:159], 0, s[72:73]
	s_waitcnt vmcnt(23)
	s_waitcnt lgkmcnt(5)
	v_mfma_f32_32x32x16_f16 v[2:17], v[122:125], v[58:61], v[2:17]
	s_waitcnt lgkmcnt(4)
	v_mfma_f32_32x32x16_f16 v[18:33], v[126:129], v[58:61], v[18:33]
	ds_read_b128 v[122:125], v162 offset:17536
	ds_read_b128 v[126:129], v162 offset:26240
	global_load_dwordx4 v[58:61], v[158:159], off
	v_lshl_add_u64 v[158:159], v[158:159], 0, s[72:73]
	s_waitcnt vmcnt(23)
	s_waitcnt lgkmcnt(5)
	v_mfma_f32_32x32x16_f16 v[2:17], v[130:133], v[54:57], v[2:17]
	s_waitcnt lgkmcnt(4)
	v_mfma_f32_32x32x16_f16 v[18:33], v[134:137], v[54:57], v[18:33]
	ds_read_b128 v[130:133], v162 offset:17568
	ds_read_b128 v[134:137], v162 offset:26272
	global_load_dwordx4 v[54:57], v[158:159], off
	v_lshl_add_u64 v[158:159], v[158:159], 0, s[72:73]
	s_waitcnt vmcnt(23)
	s_waitcnt lgkmcnt(5)
	v_mfma_f32_32x32x16_f16 v[2:17], v[114:117], v[50:53], v[2:17]
	s_waitcnt lgkmcnt(4)
	v_mfma_f32_32x32x16_f16 v[18:33], v[118:121], v[50:53], v[18:33]
	ds_read_b128 v[114:117], v162 offset:17600
	ds_read_b128 v[118:121], v162 offset:26304
	global_load_dwordx4 v[50:53], v[158:159], off
	v_lshl_add_u64 v[158:159], v[158:159], 0, s[72:73]
	s_waitcnt vmcnt(23)
	s_waitcnt lgkmcnt(5)
	v_mfma_f32_32x32x16_f16 v[2:17], v[122:125], v[46:49], v[2:17]
	s_waitcnt lgkmcnt(4)
	v_mfma_f32_32x32x16_f16 v[18:33], v[126:129], v[46:49], v[18:33]
	ds_read_b128 v[122:125], v162 offset:17632
	ds_read_b128 v[126:129], v162 offset:26336
	global_load_dwordx4 v[46:49], v[158:159], off
	v_lshl_add_u64 v[158:159], v[158:159], 0, s[72:73]
	s_waitcnt vmcnt(23)
	s_waitcnt lgkmcnt(5)
	v_mfma_f32_32x32x16_f16 v[2:17], v[130:133], v[42:45], v[2:17]
	s_waitcnt lgkmcnt(4)
	v_mfma_f32_32x32x16_f16 v[18:33], v[134:137], v[42:45], v[18:33]
	global_load_dwordx4 v[42:45], v[158:159], off
	v_lshl_add_u64 v[158:159], v[158:159], 0, s[72:73]
	s_waitcnt vmcnt(23)
	s_waitcnt lgkmcnt(3)
	v_mfma_f32_32x32x16_f16 v[2:17], v[114:117], v[38:41], v[2:17]
	s_waitcnt lgkmcnt(2)
	v_mfma_f32_32x32x16_f16 v[18:33], v[118:121], v[38:41], v[18:33]
	global_load_dwordx4 v[38:41], v[158:159], off
	v_lshl_add_u64 v[158:159], v[158:159], 0, s[72:73]
	s_waitcnt vmcnt(23)
	s_waitcnt lgkmcnt(1)
	v_mfma_f32_32x32x16_f16 v[2:17], v[122:125], v[34:37], v[2:17]
	s_waitcnt lgkmcnt(0)
	v_mfma_f32_32x32x16_f16 v[18:33], v[126:129], v[34:37], v[18:33]
	global_load_dwordx4 v[34:37], v[158:159], off
	v_lshl_add_u64 v[158:159], v[158:159], 0, s[72:73]
	s_waitcnt lgkmcnt(0)
	s_barrier
	ds_read_b128 v[114:117], v162 offset:34816
	ds_read_b128 v[118:121], v162 offset:43520
	ds_read_b128 v[122:125], v162 offset:34848
	ds_read_b128 v[126:129], v162 offset:43552
	ds_read_b128 v[130:133], v162 offset:34880
	ds_read_b128 v[134:137], v162 offset:43584
	s_waitcnt vmcnt(23)
	s_waitcnt lgkmcnt(5)
	v_mfma_f32_32x32x16_f16 v[2:17], v[114:117], v[94:97], v[2:17]
	s_waitcnt lgkmcnt(4)
	v_mfma_f32_32x32x16_f16 v[18:33], v[118:121], v[94:97], v[18:33]
	ds_read_b128 v[114:117], v162 offset:34912
	ds_read_b128 v[118:121], v162 offset:43616
	global_load_dwordx4 v[94:97], v[158:159], off
	v_lshl_add_u64 v[158:159], v[158:159], 0, s[72:73]
	s_waitcnt vmcnt(23)
	s_waitcnt lgkmcnt(5)
	v_mfma_f32_32x32x16_f16 v[2:17], v[122:125], v[98:101], v[2:17]
	s_waitcnt lgkmcnt(4)
	v_mfma_f32_32x32x16_f16 v[18:33], v[126:129], v[98:101], v[18:33]
	ds_read_b128 v[122:125], v162 offset:34944
	ds_read_b128 v[126:129], v162 offset:43648
	global_load_dwordx4 v[98:101], v[158:159], off
	v_lshl_add_u64 v[158:159], v[158:159], 0, s[72:73]
	s_waitcnt vmcnt(23)
	s_waitcnt lgkmcnt(5)
	v_mfma_f32_32x32x16_f16 v[2:17], v[130:133], v[102:105], v[2:17]
	s_waitcnt lgkmcnt(4)
	v_mfma_f32_32x32x16_f16 v[18:33], v[134:137], v[102:105], v[18:33]
	ds_read_b128 v[130:133], v162 offset:34976
	ds_read_b128 v[134:137], v162 offset:43680
	global_load_dwordx4 v[102:105], v[158:159], off
	v_lshl_add_u64 v[158:159], v[158:159], 0, s[72:73]
	s_waitcnt vmcnt(23)
	s_waitcnt lgkmcnt(5)
	v_mfma_f32_32x32x16_f16 v[2:17], v[114:117], v[106:109], v[2:17]
	s_waitcnt lgkmcnt(4)
	v_mfma_f32_32x32x16_f16 v[18:33], v[118:121], v[106:109], v[18:33]
	ds_read_b128 v[114:117], v162 offset:35008
	ds_read_b128 v[118:121], v162 offset:43712
	global_load_dwordx4 v[106:109], v[158:159], off
	v_lshl_add_u64 v[158:159], v[158:159], 0, s[72:73]
	s_waitcnt vmcnt(23)
	s_waitcnt lgkmcnt(5)
	v_mfma_f32_32x32x16_f16 v[2:17], v[122:125], v[142:145], v[2:17]
	s_waitcnt lgkmcnt(4)
	v_mfma_f32_32x32x16_f16 v[18:33], v[126:129], v[142:145], v[18:33]
	ds_read_b128 v[122:125], v162 offset:35040
	ds_read_b128 v[126:129], v162 offset:43744
	global_load_dwordx4 v[142:145], v[158:159], off
	v_lshl_add_u64 v[158:159], v[158:159], 0, s[72:73]
	s_waitcnt vmcnt(23)
	s_waitcnt lgkmcnt(5)
	v_mfma_f32_32x32x16_f16 v[2:17], v[130:133], v[146:149], v[2:17]
	s_waitcnt lgkmcnt(4)
	v_mfma_f32_32x32x16_f16 v[18:33], v[134:137], v[146:149], v[18:33]
	global_load_dwordx4 v[146:149], v[158:159], off
	v_lshl_add_u64 v[158:159], v[158:159], 0, s[72:73]
	s_waitcnt vmcnt(23)
	s_waitcnt lgkmcnt(3)
	v_mfma_f32_32x32x16_f16 v[2:17], v[114:117], v[150:153], v[2:17]
	s_waitcnt lgkmcnt(2)
	v_mfma_f32_32x32x16_f16 v[18:33], v[118:121], v[150:153], v[18:33]
	global_load_dwordx4 v[150:153], v[158:159], off
	v_lshl_add_u64 v[158:159], v[158:159], 0, s[72:73]
	s_waitcnt vmcnt(23)
	s_waitcnt lgkmcnt(1)
	v_mfma_f32_32x32x16_f16 v[2:17], v[122:125], v[154:157], v[2:17]
	s_waitcnt lgkmcnt(0)
	v_mfma_f32_32x32x16_f16 v[18:33], v[126:129], v[154:157], v[18:33]
	global_load_dwordx4 v[154:157], v[158:159], off
	v_lshl_add_u64 v[158:159], v[158:159], 0, s[72:73]
	s_waitcnt lgkmcnt(0)
	s_barrier
	ds_read_b128 v[114:117], v162 offset:0
	ds_read_b128 v[118:121], v162 offset:8704
	ds_read_b128 v[122:125], v162 offset:32
	ds_read_b128 v[126:129], v162 offset:8736
	ds_read_b128 v[130:133], v162 offset:64
	ds_read_b128 v[134:137], v162 offset:8768
	s_waitcnt vmcnt(23)
	s_waitcnt lgkmcnt(5)
	v_mfma_f32_32x32x16_f16 v[2:17], v[114:117], v[110:113], v[2:17]
	s_waitcnt lgkmcnt(4)
	v_mfma_f32_32x32x16_f16 v[18:33], v[118:121], v[110:113], v[18:33]
	ds_read_b128 v[114:117], v162 offset:96
	ds_read_b128 v[118:121], v162 offset:8800
	global_load_dwordx4 v[110:113], v[158:159], off
	v_lshl_add_u64 v[158:159], v[158:159], 0, s[72:73]
	s_waitcnt vmcnt(23)
	s_waitcnt lgkmcnt(5)
	v_mfma_f32_32x32x16_f16 v[2:17], v[122:125], v[90:93], v[2:17]
	s_waitcnt lgkmcnt(4)
	v_mfma_f32_32x32x16_f16 v[18:33], v[126:129], v[90:93], v[18:33]
	ds_read_b128 v[122:125], v162 offset:128
	ds_read_b128 v[126:129], v162 offset:8832
	global_load_dwordx4 v[90:93], v[158:159], off
	v_lshl_add_u64 v[158:159], v[158:159], 0, s[72:73]
	s_waitcnt vmcnt(23)
	s_waitcnt lgkmcnt(5)
	v_mfma_f32_32x32x16_f16 v[2:17], v[130:133], v[86:89], v[2:17]
	s_waitcnt lgkmcnt(4)
	v_mfma_f32_32x32x16_f16 v[18:33], v[134:137], v[86:89], v[18:33]
	ds_read_b128 v[130:133], v162 offset:160
	ds_read_b128 v[134:137], v162 offset:8864
	global_load_dwordx4 v[86:89], v[158:159], off
	v_lshl_add_u64 v[158:159], v[158:159], 0, s[72:73]
	s_waitcnt vmcnt(23)
	s_waitcnt lgkmcnt(5)
	v_mfma_f32_32x32x16_f16 v[2:17], v[114:117], v[82:85], v[2:17]
	s_waitcnt lgkmcnt(4)
	v_mfma_f32_32x32x16_f16 v[18:33], v[118:121], v[82:85], v[18:33]
	ds_read_b128 v[114:117], v162 offset:192
	ds_read_b128 v[118:121], v162 offset:8896
	global_load_dwordx4 v[82:85], v[158:159], off
	v_lshl_add_u64 v[158:159], v[158:159], 0, s[72:73]
	s_waitcnt vmcnt(23)
	s_waitcnt lgkmcnt(5)
	v_mfma_f32_32x32x16_f16 v[2:17], v[122:125], v[78:81], v[2:17]
	s_waitcnt lgkmcnt(4)
	v_mfma_f32_32x32x16_f16 v[18:33], v[126:129], v[78:81], v[18:33]
	ds_read_b128 v[122:125], v162 offset:224
	ds_read_b128 v[126:129], v162 offset:8928
	global_load_dwordx4 v[78:81], v[158:159], off
	v_lshl_add_u64 v[158:159], v[158:159], 0, s[72:73]
	s_waitcnt vmcnt(23)
	s_waitcnt lgkmcnt(5)
	v_mfma_f32_32x32x16_f16 v[2:17], v[130:133], v[74:77], v[2:17]
	s_waitcnt lgkmcnt(4)
	v_mfma_f32_32x32x16_f16 v[18:33], v[134:137], v[74:77], v[18:33]
	global_load_dwordx4 v[74:77], v[158:159], off
	v_lshl_add_u64 v[158:159], v[158:159], 0, s[72:73]
	s_waitcnt vmcnt(23)
	s_waitcnt lgkmcnt(3)
	v_mfma_f32_32x32x16_f16 v[2:17], v[114:117], v[70:73], v[2:17]
	s_waitcnt lgkmcnt(2)
	v_mfma_f32_32x32x16_f16 v[18:33], v[118:121], v[70:73], v[18:33]
	global_load_dwordx4 v[70:73], v[158:159], off
	v_lshl_add_u64 v[158:159], v[158:159], 0, s[72:73]
	s_waitcnt vmcnt(23)
	s_waitcnt lgkmcnt(1)
	v_mfma_f32_32x32x16_f16 v[2:17], v[122:125], v[66:69], v[2:17]
	s_waitcnt lgkmcnt(0)
	v_mfma_f32_32x32x16_f16 v[18:33], v[126:129], v[66:69], v[18:33]
	global_load_dwordx4 v[66:69], v[158:159], off
	v_lshl_add_u64 v[158:159], v[158:159], 0, s[72:73]
	s_waitcnt lgkmcnt(0)
	s_barrier
	ds_read_b128 v[114:117], v162 offset:17408
	ds_read_b128 v[118:121], v162 offset:26112
	ds_read_b128 v[122:125], v162 offset:17440
	ds_read_b128 v[126:129], v162 offset:26144
	ds_read_b128 v[130:133], v162 offset:17472
	ds_read_b128 v[134:137], v162 offset:26176
	s_waitcnt vmcnt(23)
	s_waitcnt lgkmcnt(5)
	v_mfma_f32_32x32x16_f16 v[2:17], v[114:117], v[62:65], v[2:17]
	s_waitcnt lgkmcnt(4)
	v_mfma_f32_32x32x16_f16 v[18:33], v[118:121], v[62:65], v[18:33]
	ds_read_b128 v[114:117], v162 offset:17504
	ds_read_b128 v[118:121], v162 offset:26208
	global_load_dwordx4 v[62:65], v[158:159], off
	v_lshl_add_u64 v[158:159], v[158:159], 0, s[72:73]
	s_waitcnt vmcnt(23)
	s_waitcnt lgkmcnt(5)
	v_mfma_f32_32x32x16_f16 v[2:17], v[122:125], v[58:61], v[2:17]
	s_waitcnt lgkmcnt(4)
	v_mfma_f32_32x32x16_f16 v[18:33], v[126:129], v[58:61], v[18:33]
	ds_read_b128 v[122:125], v162 offset:17536
	ds_read_b128 v[126:129], v162 offset:26240
	global_load_dwordx4 v[58:61], v[158:159], off
	v_lshl_add_u64 v[158:159], v[158:159], 0, s[72:73]
	s_waitcnt vmcnt(23)
	s_waitcnt lgkmcnt(5)
	v_mfma_f32_32x32x16_f16 v[2:17], v[130:133], v[54:57], v[2:17]
	s_waitcnt lgkmcnt(4)
	v_mfma_f32_32x32x16_f16 v[18:33], v[134:137], v[54:57], v[18:33]
	ds_read_b128 v[130:133], v162 offset:17568
	ds_read_b128 v[134:137], v162 offset:26272
	global_load_dwordx4 v[54:57], v[158:159], off
	v_lshl_add_u64 v[158:159], v[158:159], 0, s[72:73]
	s_waitcnt vmcnt(23)
	s_waitcnt lgkmcnt(5)
	v_mfma_f32_32x32x16_f16 v[2:17], v[114:117], v[50:53], v[2:17]
	s_waitcnt lgkmcnt(4)
	v_mfma_f32_32x32x16_f16 v[18:33], v[118:121], v[50:53], v[18:33]
	ds_read_b128 v[114:117], v162 offset:17600
	ds_read_b128 v[118:121], v162 offset:26304
	global_load_dwordx4 v[50:53], v[158:159], off
	v_lshl_add_u64 v[158:159], v[158:159], 0, s[72:73]
	s_waitcnt vmcnt(23)
	s_waitcnt lgkmcnt(5)
	v_mfma_f32_32x32x16_f16 v[2:17], v[122:125], v[46:49], v[2:17]
	s_waitcnt lgkmcnt(4)
	v_mfma_f32_32x32x16_f16 v[18:33], v[126:129], v[46:49], v[18:33]
	ds_read_b128 v[122:125], v162 offset:17632
	ds_read_b128 v[126:129], v162 offset:26336
	global_load_dwordx4 v[46:49], v[158:159], off
	v_lshl_add_u64 v[158:159], v[158:159], 0, s[72:73]
	s_waitcnt vmcnt(23)
	s_waitcnt lgkmcnt(5)
	v_mfma_f32_32x32x16_f16 v[2:17], v[130:133], v[42:45], v[2:17]
	s_waitcnt lgkmcnt(4)
	v_mfma_f32_32x32x16_f16 v[18:33], v[134:137], v[42:45], v[18:33]
	global_load_dwordx4 v[42:45], v[158:159], off
	v_lshl_add_u64 v[158:159], v[158:159], 0, s[72:73]
	s_waitcnt vmcnt(23)
	s_waitcnt lgkmcnt(3)
	v_mfma_f32_32x32x16_f16 v[2:17], v[114:117], v[38:41], v[2:17]
	s_waitcnt lgkmcnt(2)
	v_mfma_f32_32x32x16_f16 v[18:33], v[118:121], v[38:41], v[18:33]
	global_load_dwordx4 v[38:41], v[158:159], off
	v_lshl_add_u64 v[158:159], v[158:159], 0, s[72:73]
	s_waitcnt vmcnt(23)
	s_waitcnt lgkmcnt(1)
	v_mfma_f32_32x32x16_f16 v[2:17], v[122:125], v[34:37], v[2:17]
	s_waitcnt lgkmcnt(0)
	v_mfma_f32_32x32x16_f16 v[18:33], v[126:129], v[34:37], v[18:33]
	global_load_dwordx4 v[34:37], v[158:159], off
	v_lshl_add_u64 v[158:159], v[158:159], 0, s[72:73]
	s_waitcnt lgkmcnt(0)
	s_barrier
	ds_read_b128 v[114:117], v162 offset:34816
	ds_read_b128 v[118:121], v162 offset:43520
	ds_read_b128 v[122:125], v162 offset:34848
	ds_read_b128 v[126:129], v162 offset:43552
	ds_read_b128 v[130:133], v162 offset:34880
	ds_read_b128 v[134:137], v162 offset:43584
	s_waitcnt vmcnt(23)
	s_waitcnt lgkmcnt(5)
	v_mfma_f32_32x32x16_f16 v[2:17], v[114:117], v[94:97], v[2:17]
	s_waitcnt lgkmcnt(4)
	v_mfma_f32_32x32x16_f16 v[18:33], v[118:121], v[94:97], v[18:33]
	ds_read_b128 v[114:117], v162 offset:34912
	ds_read_b128 v[118:121], v162 offset:43616
	global_load_dwordx4 v[94:97], v[158:159], off
	v_lshl_add_u64 v[158:159], v[158:159], 0, s[72:73]
	s_waitcnt vmcnt(23)
	s_waitcnt lgkmcnt(5)
	v_mfma_f32_32x32x16_f16 v[2:17], v[122:125], v[98:101], v[2:17]
	s_waitcnt lgkmcnt(4)
	v_mfma_f32_32x32x16_f16 v[18:33], v[126:129], v[98:101], v[18:33]
	ds_read_b128 v[122:125], v162 offset:34944
	ds_read_b128 v[126:129], v162 offset:43648
	global_load_dwordx4 v[98:101], v[158:159], off
	v_lshl_add_u64 v[158:159], v[158:159], 0, s[72:73]
	s_waitcnt vmcnt(23)
	s_waitcnt lgkmcnt(5)
	v_mfma_f32_32x32x16_f16 v[2:17], v[130:133], v[102:105], v[2:17]
	s_waitcnt lgkmcnt(4)
	v_mfma_f32_32x32x16_f16 v[18:33], v[134:137], v[102:105], v[18:33]
	ds_read_b128 v[130:133], v162 offset:34976
	ds_read_b128 v[134:137], v162 offset:43680
	global_load_dwordx4 v[102:105], v[158:159], off
	v_lshl_add_u64 v[158:159], v[158:159], 0, s[72:73]
	s_waitcnt vmcnt(23)
	s_waitcnt lgkmcnt(5)
	v_mfma_f32_32x32x16_f16 v[2:17], v[114:117], v[106:109], v[2:17]
	s_waitcnt lgkmcnt(4)
	v_mfma_f32_32x32x16_f16 v[18:33], v[118:121], v[106:109], v[18:33]
	ds_read_b128 v[114:117], v162 offset:35008
	ds_read_b128 v[118:121], v162 offset:43712
	global_load_dwordx4 v[106:109], v[158:159], off
	v_lshl_add_u64 v[158:159], v[158:159], 0, s[72:73]
	s_waitcnt vmcnt(23)
	s_waitcnt lgkmcnt(5)
	v_mfma_f32_32x32x16_f16 v[2:17], v[122:125], v[142:145], v[2:17]
	s_waitcnt lgkmcnt(4)
	v_mfma_f32_32x32x16_f16 v[18:33], v[126:129], v[142:145], v[18:33]
	ds_read_b128 v[122:125], v162 offset:35040
	ds_read_b128 v[126:129], v162 offset:43744
	global_load_dwordx4 v[142:145], v[158:159], off
	v_lshl_add_u64 v[158:159], v[158:159], 0, s[72:73]
	s_waitcnt vmcnt(23)
	s_waitcnt lgkmcnt(5)
	v_mfma_f32_32x32x16_f16 v[2:17], v[130:133], v[146:149], v[2:17]
	s_waitcnt lgkmcnt(4)
	v_mfma_f32_32x32x16_f16 v[18:33], v[134:137], v[146:149], v[18:33]
	global_load_dwordx4 v[146:149], v[158:159], off
	v_lshl_add_u64 v[158:159], v[158:159], 0, s[72:73]
	s_waitcnt vmcnt(23)
	s_waitcnt lgkmcnt(3)
	v_mfma_f32_32x32x16_f16 v[2:17], v[114:117], v[150:153], v[2:17]
	s_waitcnt lgkmcnt(2)
	v_mfma_f32_32x32x16_f16 v[18:33], v[118:121], v[150:153], v[18:33]
	global_load_dwordx4 v[150:153], v[158:159], off
	v_lshl_add_u64 v[158:159], v[158:159], 0, s[72:73]
	s_waitcnt vmcnt(23)
	s_waitcnt lgkmcnt(1)
	v_mfma_f32_32x32x16_f16 v[2:17], v[122:125], v[154:157], v[2:17]
	s_waitcnt lgkmcnt(0)
	v_mfma_f32_32x32x16_f16 v[18:33], v[126:129], v[154:157], v[18:33]
	global_load_dwordx4 v[154:157], v[158:159], off
	v_lshl_add_u64 v[158:159], v[158:159], 0, s[72:73]
	s_waitcnt lgkmcnt(0)
	s_barrier
	ds_read_b128 v[114:117], v162 offset:0
	ds_read_b128 v[118:121], v162 offset:8704
	ds_read_b128 v[122:125], v162 offset:32
	ds_read_b128 v[126:129], v162 offset:8736
	ds_read_b128 v[130:133], v162 offset:64
	ds_read_b128 v[134:137], v162 offset:8768
	s_waitcnt vmcnt(23)
	s_waitcnt lgkmcnt(5)
	v_mfma_f32_32x32x16_f16 v[2:17], v[114:117], v[110:113], v[2:17]
	s_waitcnt lgkmcnt(4)
	v_mfma_f32_32x32x16_f16 v[18:33], v[118:121], v[110:113], v[18:33]
	ds_read_b128 v[114:117], v162 offset:96
	ds_read_b128 v[118:121], v162 offset:8800
	global_load_dwordx4 v[110:113], v[158:159], off
	v_lshl_add_u64 v[158:159], v[158:159], 0, s[72:73]
	s_waitcnt vmcnt(23)
	s_waitcnt lgkmcnt(5)
	v_mfma_f32_32x32x16_f16 v[2:17], v[122:125], v[90:93], v[2:17]
	s_waitcnt lgkmcnt(4)
	v_mfma_f32_32x32x16_f16 v[18:33], v[126:129], v[90:93], v[18:33]
	ds_read_b128 v[122:125], v162 offset:128
	ds_read_b128 v[126:129], v162 offset:8832
	global_load_dwordx4 v[90:93], v[158:159], off
	v_lshl_add_u64 v[158:159], v[158:159], 0, s[72:73]
	s_waitcnt vmcnt(23)
	s_waitcnt lgkmcnt(5)
	v_mfma_f32_32x32x16_f16 v[2:17], v[130:133], v[86:89], v[2:17]
	s_waitcnt lgkmcnt(4)
	v_mfma_f32_32x32x16_f16 v[18:33], v[134:137], v[86:89], v[18:33]
	ds_read_b128 v[130:133], v162 offset:160
	ds_read_b128 v[134:137], v162 offset:8864
	global_load_dwordx4 v[86:89], v[158:159], off
	v_lshl_add_u64 v[158:159], v[158:159], 0, s[72:73]
	s_waitcnt vmcnt(23)
	s_waitcnt lgkmcnt(5)
	v_mfma_f32_32x32x16_f16 v[2:17], v[114:117], v[82:85], v[2:17]
	s_waitcnt lgkmcnt(4)
	v_mfma_f32_32x32x16_f16 v[18:33], v[118:121], v[82:85], v[18:33]
	ds_read_b128 v[114:117], v162 offset:192
	ds_read_b128 v[118:121], v162 offset:8896
	global_load_dwordx4 v[82:85], v[158:159], off
	v_lshl_add_u64 v[158:159], v[158:159], 0, s[72:73]
	s_waitcnt vmcnt(23)
	s_waitcnt lgkmcnt(5)
	v_mfma_f32_32x32x16_f16 v[2:17], v[122:125], v[78:81], v[2:17]
	s_waitcnt lgkmcnt(4)
	v_mfma_f32_32x32x16_f16 v[18:33], v[126:129], v[78:81], v[18:33]
	ds_read_b128 v[122:125], v162 offset:224
	ds_read_b128 v[126:129], v162 offset:8928
	global_load_dwordx4 v[78:81], v[158:159], off
	v_lshl_add_u64 v[158:159], v[158:159], 0, s[72:73]
	s_waitcnt vmcnt(23)
	s_waitcnt lgkmcnt(5)
	v_mfma_f32_32x32x16_f16 v[2:17], v[130:133], v[74:77], v[2:17]
	s_waitcnt lgkmcnt(4)
	v_mfma_f32_32x32x16_f16 v[18:33], v[134:137], v[74:77], v[18:33]
	global_load_dwordx4 v[74:77], v[158:159], off
	v_lshl_add_u64 v[158:159], v[158:159], 0, s[72:73]
	s_waitcnt vmcnt(23)
	s_waitcnt lgkmcnt(3)
	v_mfma_f32_32x32x16_f16 v[2:17], v[114:117], v[70:73], v[2:17]
	s_waitcnt lgkmcnt(2)
	v_mfma_f32_32x32x16_f16 v[18:33], v[118:121], v[70:73], v[18:33]
	global_load_dwordx4 v[70:73], v[158:159], off
	v_lshl_add_u64 v[158:159], v[158:159], 0, s[72:73]
	s_waitcnt vmcnt(23)
	s_waitcnt lgkmcnt(1)
	v_mfma_f32_32x32x16_f16 v[2:17], v[122:125], v[66:69], v[2:17]
	s_waitcnt lgkmcnt(0)
	v_mfma_f32_32x32x16_f16 v[18:33], v[126:129], v[66:69], v[18:33]
	global_load_dwordx4 v[66:69], v[158:159], off
	v_lshl_add_u64 v[158:159], v[158:159], 0, s[72:73]
	s_waitcnt lgkmcnt(0)
	s_barrier
	ds_read_b128 v[114:117], v162 offset:17408
	ds_read_b128 v[118:121], v162 offset:26112
	ds_read_b128 v[122:125], v162 offset:17440
	ds_read_b128 v[126:129], v162 offset:26144
	ds_read_b128 v[130:133], v162 offset:17472
	ds_read_b128 v[134:137], v162 offset:26176
	s_waitcnt vmcnt(23)
	s_waitcnt lgkmcnt(5)
	v_mfma_f32_32x32x16_f16 v[2:17], v[114:117], v[62:65], v[2:17]
	s_waitcnt lgkmcnt(4)
	v_mfma_f32_32x32x16_f16 v[18:33], v[118:121], v[62:65], v[18:33]
	ds_read_b128 v[114:117], v162 offset:17504
	ds_read_b128 v[118:121], v162 offset:26208
	global_load_dwordx4 v[62:65], v[158:159], off
	v_lshl_add_u64 v[158:159], v[158:159], 0, s[72:73]
	s_waitcnt vmcnt(23)
	s_waitcnt lgkmcnt(5)
	v_mfma_f32_32x32x16_f16 v[2:17], v[122:125], v[58:61], v[2:17]
	s_waitcnt lgkmcnt(4)
	v_mfma_f32_32x32x16_f16 v[18:33], v[126:129], v[58:61], v[18:33]
	ds_read_b128 v[122:125], v162 offset:17536
	ds_read_b128 v[126:129], v162 offset:26240
	global_load_dwordx4 v[58:61], v[158:159], off
	v_lshl_add_u64 v[158:159], v[158:159], 0, s[72:73]
	s_waitcnt vmcnt(23)
	s_waitcnt lgkmcnt(5)
	v_mfma_f32_32x32x16_f16 v[2:17], v[130:133], v[54:57], v[2:17]
	s_waitcnt lgkmcnt(4)
	v_mfma_f32_32x32x16_f16 v[18:33], v[134:137], v[54:57], v[18:33]
	ds_read_b128 v[130:133], v162 offset:17568
	ds_read_b128 v[134:137], v162 offset:26272
	global_load_dwordx4 v[54:57], v[158:159], off
	v_lshl_add_u64 v[158:159], v[158:159], 0, s[72:73]
	s_waitcnt vmcnt(23)
	s_waitcnt lgkmcnt(5)
	v_mfma_f32_32x32x16_f16 v[2:17], v[114:117], v[50:53], v[2:17]
	s_waitcnt lgkmcnt(4)
	v_mfma_f32_32x32x16_f16 v[18:33], v[118:121], v[50:53], v[18:33]
	ds_read_b128 v[114:117], v162 offset:17600
	ds_read_b128 v[118:121], v162 offset:26304
	global_load_dwordx4 v[50:53], v[158:159], off
	v_lshl_add_u64 v[158:159], v[158:159], 0, s[72:73]
	s_waitcnt vmcnt(23)
	s_waitcnt lgkmcnt(5)
	v_mfma_f32_32x32x16_f16 v[2:17], v[122:125], v[46:49], v[2:17]
	s_waitcnt lgkmcnt(4)
	v_mfma_f32_32x32x16_f16 v[18:33], v[126:129], v[46:49], v[18:33]
	ds_read_b128 v[122:125], v162 offset:17632
	ds_read_b128 v[126:129], v162 offset:26336
	global_load_dwordx4 v[46:49], v[158:159], off
	v_lshl_add_u64 v[158:159], v[158:159], 0, s[72:73]
	s_waitcnt vmcnt(23)
	s_waitcnt lgkmcnt(5)
	v_mfma_f32_32x32x16_f16 v[2:17], v[130:133], v[42:45], v[2:17]
	s_waitcnt lgkmcnt(4)
	v_mfma_f32_32x32x16_f16 v[18:33], v[134:137], v[42:45], v[18:33]
	global_load_dwordx4 v[42:45], v[158:159], off
	v_lshl_add_u64 v[158:159], v[158:159], 0, s[72:73]
	s_waitcnt vmcnt(23)
	s_waitcnt lgkmcnt(3)
	v_mfma_f32_32x32x16_f16 v[2:17], v[114:117], v[38:41], v[2:17]
	s_waitcnt lgkmcnt(2)
	v_mfma_f32_32x32x16_f16 v[18:33], v[118:121], v[38:41], v[18:33]
	global_load_dwordx4 v[38:41], v[158:159], off
	v_lshl_add_u64 v[158:159], v[158:159], 0, s[72:73]
	s_waitcnt vmcnt(23)
	s_waitcnt lgkmcnt(1)
	v_mfma_f32_32x32x16_f16 v[2:17], v[122:125], v[34:37], v[2:17]
	s_waitcnt lgkmcnt(0)
	v_mfma_f32_32x32x16_f16 v[18:33], v[126:129], v[34:37], v[18:33]
	global_load_dwordx4 v[34:37], v[158:159], off
	v_lshl_add_u64 v[158:159], v[158:159], 0, s[72:73]
	s_waitcnt lgkmcnt(0)
	s_barrier
	ds_read_b128 v[114:117], v162 offset:34816
	ds_read_b128 v[118:121], v162 offset:43520
	ds_read_b128 v[122:125], v162 offset:34848
	ds_read_b128 v[126:129], v162 offset:43552
	ds_read_b128 v[130:133], v162 offset:34880
	ds_read_b128 v[134:137], v162 offset:43584
	s_waitcnt vmcnt(23)
	s_waitcnt lgkmcnt(5)
	v_mfma_f32_32x32x16_f16 v[2:17], v[114:117], v[94:97], v[2:17]
	s_waitcnt lgkmcnt(4)
	v_mfma_f32_32x32x16_f16 v[18:33], v[118:121], v[94:97], v[18:33]
	ds_read_b128 v[114:117], v162 offset:34912
	ds_read_b128 v[118:121], v162 offset:43616
	global_load_dwordx4 v[94:97], v[158:159], off
	v_lshl_add_u64 v[158:159], v[158:159], 0, s[72:73]
	s_waitcnt vmcnt(23)
	s_waitcnt lgkmcnt(5)
	v_mfma_f32_32x32x16_f16 v[2:17], v[122:125], v[98:101], v[2:17]
	s_waitcnt lgkmcnt(4)
	v_mfma_f32_32x32x16_f16 v[18:33], v[126:129], v[98:101], v[18:33]
	ds_read_b128 v[122:125], v162 offset:34944
	ds_read_b128 v[126:129], v162 offset:43648
	global_load_dwordx4 v[98:101], v[158:159], off
	v_lshl_add_u64 v[158:159], v[158:159], 0, s[72:73]
	s_waitcnt vmcnt(23)
	s_waitcnt lgkmcnt(5)
	v_mfma_f32_32x32x16_f16 v[2:17], v[130:133], v[102:105], v[2:17]
	s_waitcnt lgkmcnt(4)
	v_mfma_f32_32x32x16_f16 v[18:33], v[134:137], v[102:105], v[18:33]
	ds_read_b128 v[130:133], v162 offset:34976
	ds_read_b128 v[134:137], v162 offset:43680
	global_load_dwordx4 v[102:105], v[158:159], off
	v_lshl_add_u64 v[158:159], v[158:159], 0, s[72:73]
	s_waitcnt vmcnt(23)
	s_waitcnt lgkmcnt(5)
	v_mfma_f32_32x32x16_f16 v[2:17], v[114:117], v[106:109], v[2:17]
	s_waitcnt lgkmcnt(4)
	v_mfma_f32_32x32x16_f16 v[18:33], v[118:121], v[106:109], v[18:33]
	ds_read_b128 v[114:117], v162 offset:35008
	ds_read_b128 v[118:121], v162 offset:43712
	global_load_dwordx4 v[106:109], v[158:159], off
	v_lshl_add_u64 v[158:159], v[158:159], 0, s[72:73]
	s_waitcnt vmcnt(23)
	s_waitcnt lgkmcnt(5)
	v_mfma_f32_32x32x16_f16 v[2:17], v[122:125], v[142:145], v[2:17]
	s_waitcnt lgkmcnt(4)
	v_mfma_f32_32x32x16_f16 v[18:33], v[126:129], v[142:145], v[18:33]
	ds_read_b128 v[122:125], v162 offset:35040
	ds_read_b128 v[126:129], v162 offset:43744
	global_load_dwordx4 v[142:145], v[158:159], off
	v_lshl_add_u64 v[158:159], v[158:159], 0, s[72:73]
	s_waitcnt vmcnt(23)
	s_waitcnt lgkmcnt(5)
	v_mfma_f32_32x32x16_f16 v[2:17], v[130:133], v[146:149], v[2:17]
	s_waitcnt lgkmcnt(4)
	v_mfma_f32_32x32x16_f16 v[18:33], v[134:137], v[146:149], v[18:33]
	global_load_dwordx4 v[146:149], v[158:159], off
	v_lshl_add_u64 v[158:159], v[158:159], 0, s[72:73]
	s_waitcnt vmcnt(23)
	s_waitcnt lgkmcnt(3)
	v_mfma_f32_32x32x16_f16 v[2:17], v[114:117], v[150:153], v[2:17]
	s_waitcnt lgkmcnt(2)
	v_mfma_f32_32x32x16_f16 v[18:33], v[118:121], v[150:153], v[18:33]
	global_load_dwordx4 v[150:153], v[158:159], off
	v_lshl_add_u64 v[158:159], v[158:159], 0, s[72:73]
	s_waitcnt vmcnt(23)
	s_waitcnt lgkmcnt(1)
	v_mfma_f32_32x32x16_f16 v[2:17], v[122:125], v[154:157], v[2:17]
	s_waitcnt lgkmcnt(0)
	v_mfma_f32_32x32x16_f16 v[18:33], v[126:129], v[154:157], v[18:33]
	global_load_dwordx4 v[154:157], v[158:159], off
	v_lshl_add_u64 v[158:159], v[158:159], 0, s[72:73]
	s_waitcnt lgkmcnt(0)
	s_barrier
	ds_read_b128 v[114:117], v162 offset:0
	ds_read_b128 v[118:121], v162 offset:8704
	ds_read_b128 v[122:125], v162 offset:32
	ds_read_b128 v[126:129], v162 offset:8736
	ds_read_b128 v[130:133], v162 offset:64
	ds_read_b128 v[134:137], v162 offset:8768
	s_waitcnt vmcnt(23)
	s_waitcnt lgkmcnt(5)
	v_mfma_f32_32x32x16_f16 v[2:17], v[114:117], v[110:113], v[2:17]
	s_waitcnt lgkmcnt(4)
	v_mfma_f32_32x32x16_f16 v[18:33], v[118:121], v[110:113], v[18:33]
	ds_read_b128 v[114:117], v162 offset:96
	ds_read_b128 v[118:121], v162 offset:8800
	global_load_dwordx4 v[110:113], v[158:159], off
	v_lshl_add_u64 v[158:159], v[158:159], 0, s[72:73]
	s_waitcnt vmcnt(23)
	s_waitcnt lgkmcnt(5)
	v_mfma_f32_32x32x16_f16 v[2:17], v[122:125], v[90:93], v[2:17]
	s_waitcnt lgkmcnt(4)
	v_mfma_f32_32x32x16_f16 v[18:33], v[126:129], v[90:93], v[18:33]
	ds_read_b128 v[122:125], v162 offset:128
	ds_read_b128 v[126:129], v162 offset:8832
	global_load_dwordx4 v[90:93], v[158:159], off
	v_lshl_add_u64 v[158:159], v[158:159], 0, s[72:73]
	s_waitcnt vmcnt(23)
	s_waitcnt lgkmcnt(5)
	v_mfma_f32_32x32x16_f16 v[2:17], v[130:133], v[86:89], v[2:17]
	s_waitcnt lgkmcnt(4)
	v_mfma_f32_32x32x16_f16 v[18:33], v[134:137], v[86:89], v[18:33]
	ds_read_b128 v[130:133], v162 offset:160
	ds_read_b128 v[134:137], v162 offset:8864
	global_load_dwordx4 v[86:89], v[158:159], off
	v_lshl_add_u64 v[158:159], v[158:159], 0, s[72:73]
	s_waitcnt vmcnt(23)
	s_waitcnt lgkmcnt(5)
	v_mfma_f32_32x32x16_f16 v[2:17], v[114:117], v[82:85], v[2:17]
	s_waitcnt lgkmcnt(4)
	v_mfma_f32_32x32x16_f16 v[18:33], v[118:121], v[82:85], v[18:33]
	ds_read_b128 v[114:117], v162 offset:192
	ds_read_b128 v[118:121], v162 offset:8896
	global_load_dwordx4 v[82:85], v[158:159], off
	v_lshl_add_u64 v[158:159], v[158:159], 0, s[72:73]
	s_waitcnt vmcnt(23)
	s_waitcnt lgkmcnt(5)
	v_mfma_f32_32x32x16_f16 v[2:17], v[122:125], v[78:81], v[2:17]
	s_waitcnt lgkmcnt(4)
	v_mfma_f32_32x32x16_f16 v[18:33], v[126:129], v[78:81], v[18:33]
	ds_read_b128 v[122:125], v162 offset:224
	ds_read_b128 v[126:129], v162 offset:8928
	global_load_dwordx4 v[78:81], v[158:159], off
	v_lshl_add_u64 v[158:159], v[158:159], 0, s[72:73]
	s_waitcnt vmcnt(23)
	s_waitcnt lgkmcnt(5)
	v_mfma_f32_32x32x16_f16 v[2:17], v[130:133], v[74:77], v[2:17]
	s_waitcnt lgkmcnt(4)
	v_mfma_f32_32x32x16_f16 v[18:33], v[134:137], v[74:77], v[18:33]
	global_load_dwordx4 v[74:77], v[158:159], off
	v_lshl_add_u64 v[158:159], v[158:159], 0, s[72:73]
	s_waitcnt vmcnt(23)
	s_waitcnt lgkmcnt(3)
	v_mfma_f32_32x32x16_f16 v[2:17], v[114:117], v[70:73], v[2:17]
	s_waitcnt lgkmcnt(2)
	v_mfma_f32_32x32x16_f16 v[18:33], v[118:121], v[70:73], v[18:33]
	global_load_dwordx4 v[70:73], v[158:159], off
	v_lshl_add_u64 v[158:159], v[158:159], 0, s[72:73]
	s_waitcnt vmcnt(23)
	s_waitcnt lgkmcnt(1)
	v_mfma_f32_32x32x16_f16 v[2:17], v[122:125], v[66:69], v[2:17]
	s_waitcnt lgkmcnt(0)
	v_mfma_f32_32x32x16_f16 v[18:33], v[126:129], v[66:69], v[18:33]
	global_load_dwordx4 v[66:69], v[158:159], off
	v_lshl_add_u64 v[158:159], v[158:159], 0, s[72:73]
	s_waitcnt lgkmcnt(0)
	s_barrier
	ds_read_b128 v[114:117], v162 offset:17408
	ds_read_b128 v[118:121], v162 offset:26112
	ds_read_b128 v[122:125], v162 offset:17440
	ds_read_b128 v[126:129], v162 offset:26144
	ds_read_b128 v[130:133], v162 offset:17472
	ds_read_b128 v[134:137], v162 offset:26176
	s_waitcnt vmcnt(23)
	s_waitcnt lgkmcnt(5)
	v_mfma_f32_32x32x16_f16 v[2:17], v[114:117], v[62:65], v[2:17]
	s_waitcnt lgkmcnt(4)
	v_mfma_f32_32x32x16_f16 v[18:33], v[118:121], v[62:65], v[18:33]
	ds_read_b128 v[114:117], v162 offset:17504
	ds_read_b128 v[118:121], v162 offset:26208
	global_load_dwordx4 v[62:65], v[158:159], off
	v_lshl_add_u64 v[158:159], v[158:159], 0, s[72:73]
	s_waitcnt vmcnt(23)
	s_waitcnt lgkmcnt(5)
	v_mfma_f32_32x32x16_f16 v[2:17], v[122:125], v[58:61], v[2:17]
	s_waitcnt lgkmcnt(4)
	v_mfma_f32_32x32x16_f16 v[18:33], v[126:129], v[58:61], v[18:33]
	ds_read_b128 v[122:125], v162 offset:17536
	ds_read_b128 v[126:129], v162 offset:26240
	global_load_dwordx4 v[58:61], v[158:159], off
	v_lshl_add_u64 v[158:159], v[158:159], 0, s[72:73]
	s_waitcnt vmcnt(23)
	s_waitcnt lgkmcnt(5)
	v_mfma_f32_32x32x16_f16 v[2:17], v[130:133], v[54:57], v[2:17]
	s_waitcnt lgkmcnt(4)
	v_mfma_f32_32x32x16_f16 v[18:33], v[134:137], v[54:57], v[18:33]
	ds_read_b128 v[130:133], v162 offset:17568
	ds_read_b128 v[134:137], v162 offset:26272
	global_load_dwordx4 v[54:57], v[158:159], off
	v_lshl_add_u64 v[158:159], v[158:159], 0, s[72:73]
	s_waitcnt vmcnt(23)
	s_waitcnt lgkmcnt(5)
	v_mfma_f32_32x32x16_f16 v[2:17], v[114:117], v[50:53], v[2:17]
	s_waitcnt lgkmcnt(4)
	v_mfma_f32_32x32x16_f16 v[18:33], v[118:121], v[50:53], v[18:33]
	ds_read_b128 v[114:117], v162 offset:17600
	ds_read_b128 v[118:121], v162 offset:26304
	global_load_dwordx4 v[50:53], v[158:159], off
	v_lshl_add_u64 v[158:159], v[158:159], 0, s[72:73]
	s_waitcnt vmcnt(23)
	s_waitcnt lgkmcnt(5)
	v_mfma_f32_32x32x16_f16 v[2:17], v[122:125], v[46:49], v[2:17]
	s_waitcnt lgkmcnt(4)
	v_mfma_f32_32x32x16_f16 v[18:33], v[126:129], v[46:49], v[18:33]
	ds_read_b128 v[122:125], v162 offset:17632
	ds_read_b128 v[126:129], v162 offset:26336
	global_load_dwordx4 v[46:49], v[158:159], off
	v_lshl_add_u64 v[158:159], v[158:159], 0, s[72:73]
	s_waitcnt vmcnt(23)
	s_waitcnt lgkmcnt(5)
	v_mfma_f32_32x32x16_f16 v[2:17], v[130:133], v[42:45], v[2:17]
	s_waitcnt lgkmcnt(4)
	v_mfma_f32_32x32x16_f16 v[18:33], v[134:137], v[42:45], v[18:33]
	global_load_dwordx4 v[42:45], v[158:159], off
	v_lshl_add_u64 v[158:159], v[158:159], 0, s[72:73]
	s_waitcnt vmcnt(23)
	s_waitcnt lgkmcnt(3)
	v_mfma_f32_32x32x16_f16 v[2:17], v[114:117], v[38:41], v[2:17]
	s_waitcnt lgkmcnt(2)
	v_mfma_f32_32x32x16_f16 v[18:33], v[118:121], v[38:41], v[18:33]
	global_load_dwordx4 v[38:41], v[158:159], off
	v_lshl_add_u64 v[158:159], v[158:159], 0, s[72:73]
	s_waitcnt vmcnt(23)
	s_waitcnt lgkmcnt(1)
	v_mfma_f32_32x32x16_f16 v[2:17], v[122:125], v[34:37], v[2:17]
	s_waitcnt lgkmcnt(0)
	v_mfma_f32_32x32x16_f16 v[18:33], v[126:129], v[34:37], v[18:33]
	global_load_dwordx4 v[34:37], v[158:159], off
	v_lshl_add_u64 v[158:159], v[158:159], 0, s[72:73]
	s_waitcnt lgkmcnt(0)
	s_barrier
	ds_read_b128 v[114:117], v162 offset:34816
	ds_read_b128 v[118:121], v162 offset:43520
	ds_read_b128 v[122:125], v162 offset:34848
	ds_read_b128 v[126:129], v162 offset:43552
	ds_read_b128 v[130:133], v162 offset:34880
	ds_read_b128 v[134:137], v162 offset:43584
	s_waitcnt vmcnt(23)
	s_waitcnt lgkmcnt(5)
	v_mfma_f32_32x32x16_f16 v[2:17], v[114:117], v[94:97], v[2:17]
	s_waitcnt lgkmcnt(4)
	v_mfma_f32_32x32x16_f16 v[18:33], v[118:121], v[94:97], v[18:33]
	ds_read_b128 v[114:117], v162 offset:34912
	ds_read_b128 v[118:121], v162 offset:43616
	global_load_dwordx4 v[94:97], v[158:159], off
	v_lshl_add_u64 v[158:159], v[158:159], 0, s[72:73]
	s_waitcnt vmcnt(23)
	s_waitcnt lgkmcnt(5)
	v_mfma_f32_32x32x16_f16 v[2:17], v[122:125], v[98:101], v[2:17]
	s_waitcnt lgkmcnt(4)
	v_mfma_f32_32x32x16_f16 v[18:33], v[126:129], v[98:101], v[18:33]
	ds_read_b128 v[122:125], v162 offset:34944
	ds_read_b128 v[126:129], v162 offset:43648
	global_load_dwordx4 v[98:101], v[158:159], off
	v_lshl_add_u64 v[158:159], v[158:159], 0, s[72:73]
	s_waitcnt vmcnt(23)
	s_waitcnt lgkmcnt(5)
	v_mfma_f32_32x32x16_f16 v[2:17], v[130:133], v[102:105], v[2:17]
	s_waitcnt lgkmcnt(4)
	v_mfma_f32_32x32x16_f16 v[18:33], v[134:137], v[102:105], v[18:33]
	ds_read_b128 v[130:133], v162 offset:34976
	ds_read_b128 v[134:137], v162 offset:43680
	global_load_dwordx4 v[102:105], v[158:159], off
	v_lshl_add_u64 v[158:159], v[158:159], 0, s[72:73]
	s_waitcnt vmcnt(23)
	s_waitcnt lgkmcnt(5)
	v_mfma_f32_32x32x16_f16 v[2:17], v[114:117], v[106:109], v[2:17]
	s_waitcnt lgkmcnt(4)
	v_mfma_f32_32x32x16_f16 v[18:33], v[118:121], v[106:109], v[18:33]
	ds_read_b128 v[114:117], v162 offset:35008
	ds_read_b128 v[118:121], v162 offset:43712
	global_load_dwordx4 v[106:109], v[158:159], off
	v_lshl_add_u64 v[158:159], v[158:159], 0, s[72:73]
	s_waitcnt vmcnt(23)
	s_waitcnt lgkmcnt(5)
	v_mfma_f32_32x32x16_f16 v[2:17], v[122:125], v[142:145], v[2:17]
	s_waitcnt lgkmcnt(4)
	v_mfma_f32_32x32x16_f16 v[18:33], v[126:129], v[142:145], v[18:33]
	ds_read_b128 v[122:125], v162 offset:35040
	ds_read_b128 v[126:129], v162 offset:43744
	global_load_dwordx4 v[142:145], v[158:159], off
	v_lshl_add_u64 v[158:159], v[158:159], 0, s[72:73]
	s_waitcnt vmcnt(23)
	s_waitcnt lgkmcnt(5)
	v_mfma_f32_32x32x16_f16 v[2:17], v[130:133], v[146:149], v[2:17]
	s_waitcnt lgkmcnt(4)
	v_mfma_f32_32x32x16_f16 v[18:33], v[134:137], v[146:149], v[18:33]
	global_load_dwordx4 v[146:149], v[158:159], off
	v_lshl_add_u64 v[158:159], v[158:159], 0, s[72:73]
	s_waitcnt vmcnt(23)
	s_waitcnt lgkmcnt(3)
	v_mfma_f32_32x32x16_f16 v[2:17], v[114:117], v[150:153], v[2:17]
	s_waitcnt lgkmcnt(2)
	v_mfma_f32_32x32x16_f16 v[18:33], v[118:121], v[150:153], v[18:33]
	global_load_dwordx4 v[150:153], v[158:159], off
	v_lshl_add_u64 v[158:159], v[158:159], 0, s[72:73]
	s_waitcnt vmcnt(23)
	s_waitcnt lgkmcnt(1)
	v_mfma_f32_32x32x16_f16 v[2:17], v[122:125], v[154:157], v[2:17]
	s_waitcnt lgkmcnt(0)
	v_mfma_f32_32x32x16_f16 v[18:33], v[126:129], v[154:157], v[18:33]
	global_load_dwordx4 v[154:157], v[158:159], off
	v_lshl_add_u64 v[158:159], v[158:159], 0, s[72:73]
	s_waitcnt lgkmcnt(0)
	s_barrier
	ds_read_b128 v[114:117], v162 offset:0
	ds_read_b128 v[118:121], v162 offset:8704
	ds_read_b128 v[122:125], v162 offset:32
	ds_read_b128 v[126:129], v162 offset:8736
	ds_read_b128 v[130:133], v162 offset:64
	ds_read_b128 v[134:137], v162 offset:8768
	s_waitcnt vmcnt(23)
	s_waitcnt lgkmcnt(5)
	v_mfma_f32_32x32x16_f16 v[2:17], v[114:117], v[110:113], v[2:17]
	s_waitcnt lgkmcnt(4)
	v_mfma_f32_32x32x16_f16 v[18:33], v[118:121], v[110:113], v[18:33]
	ds_read_b128 v[114:117], v162 offset:96
	ds_read_b128 v[118:121], v162 offset:8800
	s_waitcnt vmcnt(22)
	s_waitcnt lgkmcnt(5)
	v_mfma_f32_32x32x16_f16 v[2:17], v[122:125], v[90:93], v[2:17]
	s_waitcnt lgkmcnt(4)
	v_mfma_f32_32x32x16_f16 v[18:33], v[126:129], v[90:93], v[18:33]
	ds_read_b128 v[122:125], v162 offset:128
	ds_read_b128 v[126:129], v162 offset:8832
	s_waitcnt vmcnt(21)
	s_waitcnt lgkmcnt(5)
	v_mfma_f32_32x32x16_f16 v[2:17], v[130:133], v[86:89], v[2:17]
	s_waitcnt lgkmcnt(4)
	v_mfma_f32_32x32x16_f16 v[18:33], v[134:137], v[86:89], v[18:33]
	ds_read_b128 v[130:133], v162 offset:160
	ds_read_b128 v[134:137], v162 offset:8864
	s_waitcnt vmcnt(20)
	s_waitcnt lgkmcnt(5)
	v_mfma_f32_32x32x16_f16 v[2:17], v[114:117], v[82:85], v[2:17]
	s_waitcnt lgkmcnt(4)
	v_mfma_f32_32x32x16_f16 v[18:33], v[118:121], v[82:85], v[18:33]
	ds_read_b128 v[114:117], v162 offset:192
	ds_read_b128 v[118:121], v162 offset:8896
	s_waitcnt vmcnt(19)
	s_waitcnt lgkmcnt(5)
	v_mfma_f32_32x32x16_f16 v[2:17], v[122:125], v[78:81], v[2:17]
	s_waitcnt lgkmcnt(4)
	v_mfma_f32_32x32x16_f16 v[18:33], v[126:129], v[78:81], v[18:33]
	ds_read_b128 v[122:125], v162 offset:224
	ds_read_b128 v[126:129], v162 offset:8928
	s_waitcnt vmcnt(18)
	s_waitcnt lgkmcnt(5)
	v_mfma_f32_32x32x16_f16 v[2:17], v[130:133], v[74:77], v[2:17]
	s_waitcnt lgkmcnt(4)
	v_mfma_f32_32x32x16_f16 v[18:33], v[134:137], v[74:77], v[18:33]
	s_waitcnt vmcnt(17)
	s_waitcnt lgkmcnt(3)
	v_mfma_f32_32x32x16_f16 v[2:17], v[114:117], v[70:73], v[2:17]
	s_waitcnt lgkmcnt(2)
	v_mfma_f32_32x32x16_f16 v[18:33], v[118:121], v[70:73], v[18:33]
	s_waitcnt vmcnt(16)
	s_waitcnt lgkmcnt(1)
	v_mfma_f32_32x32x16_f16 v[2:17], v[122:125], v[66:69], v[2:17]
	s_waitcnt lgkmcnt(0)
	v_mfma_f32_32x32x16_f16 v[18:33], v[126:129], v[66:69], v[18:33]
	s_waitcnt lgkmcnt(0)
	s_barrier
	ds_read_b128 v[114:117], v162 offset:17408
	ds_read_b128 v[118:121], v162 offset:26112
	ds_read_b128 v[122:125], v162 offset:17440
	ds_read_b128 v[126:129], v162 offset:26144
	ds_read_b128 v[130:133], v162 offset:17472
	ds_read_b128 v[134:137], v162 offset:26176
	s_waitcnt vmcnt(15)
	s_waitcnt lgkmcnt(5)
	v_mfma_f32_32x32x16_f16 v[2:17], v[114:117], v[62:65], v[2:17]
	s_waitcnt lgkmcnt(4)
	v_mfma_f32_32x32x16_f16 v[18:33], v[118:121], v[62:65], v[18:33]
	ds_read_b128 v[114:117], v162 offset:17504
	ds_read_b128 v[118:121], v162 offset:26208
	s_waitcnt vmcnt(14)
	s_waitcnt lgkmcnt(5)
	v_mfma_f32_32x32x16_f16 v[2:17], v[122:125], v[58:61], v[2:17]
	s_waitcnt lgkmcnt(4)
	v_mfma_f32_32x32x16_f16 v[18:33], v[126:129], v[58:61], v[18:33]
	ds_read_b128 v[122:125], v162 offset:17536
	ds_read_b128 v[126:129], v162 offset:26240
	s_waitcnt vmcnt(13)
	s_waitcnt lgkmcnt(5)
	v_mfma_f32_32x32x16_f16 v[2:17], v[130:133], v[54:57], v[2:17]
	s_waitcnt lgkmcnt(4)
	v_mfma_f32_32x32x16_f16 v[18:33], v[134:137], v[54:57], v[18:33]
	ds_read_b128 v[130:133], v162 offset:17568
	ds_read_b128 v[134:137], v162 offset:26272
	s_waitcnt vmcnt(12)
	s_waitcnt lgkmcnt(5)
	v_mfma_f32_32x32x16_f16 v[2:17], v[114:117], v[50:53], v[2:17]
	s_waitcnt lgkmcnt(4)
	v_mfma_f32_32x32x16_f16 v[18:33], v[118:121], v[50:53], v[18:33]
	ds_read_b128 v[114:117], v162 offset:17600
	ds_read_b128 v[118:121], v162 offset:26304
	s_waitcnt vmcnt(11)
	s_waitcnt lgkmcnt(5)
	v_mfma_f32_32x32x16_f16 v[2:17], v[122:125], v[46:49], v[2:17]
	s_waitcnt lgkmcnt(4)
	v_mfma_f32_32x32x16_f16 v[18:33], v[126:129], v[46:49], v[18:33]
	ds_read_b128 v[122:125], v162 offset:17632
	ds_read_b128 v[126:129], v162 offset:26336
	s_waitcnt vmcnt(10)
	s_waitcnt lgkmcnt(5)
	v_mfma_f32_32x32x16_f16 v[2:17], v[130:133], v[42:45], v[2:17]
	s_waitcnt lgkmcnt(4)
	v_mfma_f32_32x32x16_f16 v[18:33], v[134:137], v[42:45], v[18:33]
	s_waitcnt vmcnt(9)
	s_waitcnt lgkmcnt(3)
	v_mfma_f32_32x32x16_f16 v[2:17], v[114:117], v[38:41], v[2:17]
	s_waitcnt lgkmcnt(2)
	v_mfma_f32_32x32x16_f16 v[18:33], v[118:121], v[38:41], v[18:33]
	s_waitcnt vmcnt(8)
	s_waitcnt lgkmcnt(1)
	v_mfma_f32_32x32x16_f16 v[2:17], v[122:125], v[34:37], v[2:17]
	s_waitcnt lgkmcnt(0)
	v_mfma_f32_32x32x16_f16 v[18:33], v[126:129], v[34:37], v[18:33]
	s_waitcnt lgkmcnt(0)
	s_barrier
	ds_read_b128 v[114:117], v162 offset:34816
	ds_read_b128 v[118:121], v162 offset:43520
	ds_read_b128 v[122:125], v162 offset:34848
	ds_read_b128 v[126:129], v162 offset:43552
	ds_read_b128 v[130:133], v162 offset:34880
	ds_read_b128 v[134:137], v162 offset:43584
	s_waitcnt vmcnt(7)
	s_waitcnt lgkmcnt(5)
	v_mfma_f32_32x32x16_f16 v[2:17], v[114:117], v[94:97], v[2:17]
	s_waitcnt lgkmcnt(4)
	v_mfma_f32_32x32x16_f16 v[18:33], v[118:121], v[94:97], v[18:33]
	ds_read_b128 v[114:117], v162 offset:34912
	ds_read_b128 v[118:121], v162 offset:43616
	s_waitcnt vmcnt(6)
	s_waitcnt lgkmcnt(5)
	v_mfma_f32_32x32x16_f16 v[2:17], v[122:125], v[98:101], v[2:17]
	s_waitcnt lgkmcnt(4)
	v_mfma_f32_32x32x16_f16 v[18:33], v[126:129], v[98:101], v[18:33]
	ds_read_b128 v[122:125], v162 offset:34944
	ds_read_b128 v[126:129], v162 offset:43648
	s_waitcnt vmcnt(5)
	s_waitcnt lgkmcnt(5)
	v_mfma_f32_32x32x16_f16 v[2:17], v[130:133], v[102:105], v[2:17]
	s_waitcnt lgkmcnt(4)
	v_mfma_f32_32x32x16_f16 v[18:33], v[134:137], v[102:105], v[18:33]
	ds_read_b128 v[130:133], v162 offset:34976
	ds_read_b128 v[134:137], v162 offset:43680
	s_waitcnt vmcnt(4)
	s_waitcnt lgkmcnt(5)
	v_mfma_f32_32x32x16_f16 v[2:17], v[114:117], v[106:109], v[2:17]
	s_waitcnt lgkmcnt(4)
	v_mfma_f32_32x32x16_f16 v[18:33], v[118:121], v[106:109], v[18:33]
	ds_read_b128 v[114:117], v162 offset:35008
	ds_read_b128 v[118:121], v162 offset:43712
	s_waitcnt vmcnt(3)
	s_waitcnt lgkmcnt(5)
	v_mfma_f32_32x32x16_f16 v[2:17], v[122:125], v[142:145], v[2:17]
	s_waitcnt lgkmcnt(4)
	v_mfma_f32_32x32x16_f16 v[18:33], v[126:129], v[142:145], v[18:33]
	ds_read_b128 v[122:125], v162 offset:35040
	ds_read_b128 v[126:129], v162 offset:43744
	s_waitcnt vmcnt(2)
	s_waitcnt lgkmcnt(5)
	v_mfma_f32_32x32x16_f16 v[2:17], v[130:133], v[146:149], v[2:17]
	s_waitcnt lgkmcnt(4)
	v_mfma_f32_32x32x16_f16 v[18:33], v[134:137], v[146:149], v[18:33]
	s_waitcnt vmcnt(1)
	s_waitcnt lgkmcnt(3)
	v_mfma_f32_32x32x16_f16 v[2:17], v[114:117], v[150:153], v[2:17]
	s_waitcnt lgkmcnt(2)
	v_mfma_f32_32x32x16_f16 v[18:33], v[118:121], v[150:153], v[18:33]
	s_waitcnt vmcnt(0)
	s_waitcnt lgkmcnt(1)
	v_mfma_f32_32x32x16_f16 v[2:17], v[122:125], v[154:157], v[2:17]
	s_waitcnt lgkmcnt(0)
	v_mfma_f32_32x32x16_f16 v[18:33], v[126:129], v[154:157], v[18:33]
	s_waitcnt lgkmcnt(0)
	s_barrier
	s_mov_b32 s2, 0x3d800000
	v_mul_u32_u24_e32 v1, 0x420, v1
	v_or_b32_e32 v34, v161, v160
	v_lshlrev_b32_e32 v34, 1, v34
	v_lshl_add_u32 v1, v1, 1, v34
	s_nop 7
	s_nop 7
	v_fma_mixlo_f16 v2, v2, s2, 0
	ds_write_b16 v1, v2
	v_fma_mixlo_f16 v2, v18, s2, 0
	ds_write_b16 v1, v2 offset:16896
	v_fma_mixlo_f16 v2, v3, s2, 0
	ds_write_b16 v1, v2 offset:528
	v_fma_mixlo_f16 v2, v19, s2, 0
	ds_write_b16 v1, v2 offset:17424
	v_fma_mixlo_f16 v2, v4, s2, 0
	ds_write_b16 v1, v2 offset:1056
	v_fma_mixlo_f16 v2, v20, s2, 0
	ds_write_b16 v1, v2 offset:17952
	v_fma_mixlo_f16 v2, v5, s2, 0
	ds_write_b16 v1, v2 offset:1584
	v_fma_mixlo_f16 v2, v21, s2, 0
	ds_write_b16 v1, v2 offset:18480
	v_fma_mixlo_f16 v2, v6, s2, 0
	ds_write_b16 v1, v2 offset:4224
	v_fma_mixlo_f16 v2, v22, s2, 0
	ds_write_b16 v1, v2 offset:21120
	v_fma_mixlo_f16 v2, v7, s2, 0
	ds_write_b16 v1, v2 offset:4752
	v_fma_mixlo_f16 v2, v23, s2, 0
	ds_write_b16 v1, v2 offset:21648
	v_fma_mixlo_f16 v2, v8, s2, 0
	ds_write_b16 v1, v2 offset:5280
	v_fma_mixlo_f16 v2, v24, s2, 0
	ds_write_b16 v1, v2 offset:22176
	v_fma_mixlo_f16 v2, v9, s2, 0
	ds_write_b16 v1, v2 offset:5808
	v_fma_mixlo_f16 v2, v25, s2, 0
	ds_write_b16 v1, v2 offset:22704
	v_fma_mixlo_f16 v2, v10, s2, 0
	ds_write_b16 v1, v2 offset:8448
	v_fma_mixlo_f16 v2, v26, s2, 0
	ds_write_b16 v1, v2 offset:25344
	v_fma_mixlo_f16 v2, v11, s2, 0
	ds_write_b16 v1, v2 offset:8976
	v_fma_mixlo_f16 v2, v27, s2, 0
	ds_write_b16 v1, v2 offset:25872
	v_fma_mixlo_f16 v2, v12, s2, 0
	ds_write_b16 v1, v2 offset:9504
	v_fma_mixlo_f16 v2, v28, s2, 0
	ds_write_b16 v1, v2 offset:26400
	v_fma_mixlo_f16 v2, v13, s2, 0
	ds_write_b16 v1, v2 offset:10032
	v_fma_mixlo_f16 v2, v29, s2, 0
	ds_write_b16 v1, v2 offset:26928
	v_fma_mixlo_f16 v2, v14, s2, 0
	ds_write_b16 v1, v2 offset:12672
	v_fma_mixlo_f16 v2, v30, s2, 0
	ds_write_b16 v1, v2 offset:29568
	v_fma_mixlo_f16 v2, v15, s2, 0
	ds_write_b16 v1, v2 offset:13200
	v_fma_mixlo_f16 v2, v31, s2, 0
	ds_write_b16 v1, v2 offset:30096
	v_fma_mixlo_f16 v2, v16, s2, 0
	ds_write_b16 v1, v2 offset:13728
	v_fma_mixlo_f16 v2, v32, s2, 0
	ds_write_b16 v1, v2 offset:30624
	v_fma_mixlo_f16 v2, v17, s2, 0
	ds_write_b16 v1, v2 offset:14256
	v_fma_mixlo_f16 v2, v33, s2, 0
	ds_write_b16 v1, v2 offset:31152
	v_lshrrev_b32_e32 v1, 3, v0
	v_lshlrev_b32_e32 v0, 4, v0
	v_and_b32_e32 v4, 0x70, v0
	s_movk_i32 s2, 0x210
	v_mad_u32_u24 v12, v1, s2, v4
	s_ashr_i32 s2, s8, 31
	s_waitcnt lgkmcnt(0)
	s_barrier
	v_or_b32_e32 v6, s8, v1
	v_mov_b32_e32 v7, s2
	v_mov_b32_e32 v5, 0
	ds_read_b128 v[0:3], v12
	v_lshl_add_u64 v[4:5], s[16:17], 0, v[4:5]
	v_lshlrev_b64 v[6:7], 7, v[6:7]
	v_lshl_add_u64 v[8:9], v[4:5], 0, v[6:7]
	ds_read_b128 v[4:7], v12 offset:128
	s_mov_b32 s2, 0x200000
	s_waitcnt lgkmcnt(1)
	global_store_dwordx4 v[8:9], v[0:3], off
	s_nop 1
	v_add_co_u32_e32 v0, vcc, s2, v8
	s_nop 1
	v_addc_co_u32_e32 v1, vcc, 0, v9, vcc
	s_waitcnt lgkmcnt(0)
	global_store_dwordx4 v[0:1], v[4:7], off
	ds_read_b128 v[0:3], v12 offset:256
	ds_read_b128 v[4:7], v12 offset:384
	v_add_co_u32_e32 v10, vcc, 0x400000, v8
	s_nop 1
	v_addc_co_u32_e32 v11, vcc, 0, v9, vcc
	s_waitcnt lgkmcnt(1)
	global_store_dwordx4 v[10:11], v[0:3], off
	s_nop 1
	v_add_co_u32_e32 v0, vcc, 0x600000, v8
	s_nop 1
	v_addc_co_u32_e32 v1, vcc, 0, v9, vcc
	s_waitcnt lgkmcnt(0)
	global_store_dwordx4 v[0:1], v[4:7], off
	s_andn2_saveexec_b64 s[0:1], s[0:1]
	s_cbranch_execz .LBB1_234
.LBB1_248:
	v_and_b32_e32 v6, 31, v0
	v_bfe_u32 v7, v0, 5, 3
	s_cmp_lt_u32 s8, 0x2000
	s_cselect_b32 s50, s12, s14
	s_cselect_b32 s51, s13, s15
	s_and_b32 s0, s8, 0x1fff
	s_mul_i32 s1, s0, 0x2ee0
	s_add_u32 s50, s50, s1
	s_addc_u32 s51, s51, 0
	s_mov_b32 s52, s50
	s_mov_b32 s53, s51
	s_add_u32 s54, s50, 0x17700
	s_addc_u32 s55, s51, 0
	s_add_u32 s56, s50, 0x2ee00
	s_addc_u32 s57, s51, 0
	s_add_u32 s58, s50, 0x46500
	s_addc_u32 s59, s51, 0
	s_add_u32 s60, s50, 0x5dc00
	s_addc_u32 s61, s51, 0
	s_add_u32 s62, s50, 0x75300
	s_addc_u32 s63, s51, 0
	s_add_u32 s64, s50, 0x8ca00
	s_addc_u32 s65, s51, 0
	s_add_u32 s66, s50, 0xa4100
	s_addc_u32 s67, s51, 0
	v_and_b32_e32 v104, 3, v7
	v_lshl_add_u32 v106, v104, 1, v6
	s_movk_i32 s0, 0x2ee0
	v_mul_lo_u32 v2, v7, s0
	v_lshl_add_u32 v2, v106, 4, v2
	s_movk_i32 s0, 0x110
	v_mul_lo_u32 v3, v7, s0
	v_lshl_add_u32 v107, v106, 3, v3
	v_cmp_le_u32_e64 s[76:77], 32, v106
	v_cmp_gt_u32_e64 s[68:69], 14, v106
	s_not_b64 s[78:79], s[76:77]
	v_mov_b32_e32 v108, 0x0
	v_mov_b32_e32 v109, 0x4300
	v_cndmask_b32_e64 v108, v108, v109, s[76:77]
	v_add_u32_e32 v110, v107, v108
	v_mov_b32_e32 v108, 0x4400
	v_mov_b32_e32 v109, 0x8700
	v_cndmask_b32_e64 v108, v108, v109, s[76:77]
	v_add_u32_e32 v111, v107, v108
	v_mov_b32_e32 v108, 0x8800
	v_mov_b32_e32 v109, 0xffffff00
	v_cndmask_b32_e64 v108, v108, v109, s[76:77]
	v_add_u32_e32 v112, v107, v108
	v_mov_b32_e32 v116, 0
	v_mov_b32_e32 v117, 0
	v_mov_b32_e32 v118, 0
	v_mov_b32_e32 v119, 0
	s_mov_b64 s[70:71], exec
	s_mov_b64 exec, s[76:77]
	global_load_dwordx4 v[116:119], v2, s[52:53] offset:-512 nt
	s_mov_b64 exec, s[70:71]
	v_mov_b32_e32 v120, 0
	v_mov_b32_e32 v121, 0
	v_mov_b32_e32 v122, 0
	v_mov_b32_e32 v123, 0
	s_mov_b64 s[70:71], exec
	s_mov_b64 exec, s[76:77]
	global_load_dwordx4 v[120:123], v2, s[54:55] offset:-512 nt
	s_mov_b64 exec, s[70:71]
	v_mov_b32_e32 v124, 0
	v_mov_b32_e32 v125, 0
	v_mov_b32_e32 v126, 0
	v_mov_b32_e32 v127, 0
	s_mov_b64 s[70:71], exec
	s_mov_b64 exec, s[76:77]
	global_load_dwordx4 v[124:127], v2, s[56:57] offset:-512 nt
	s_mov_b64 exec, s[70:71]
	v_mov_b32_e32 v128, 0
	v_mov_b32_e32 v129, 0
	v_mov_b32_e32 v130, 0
	v_mov_b32_e32 v131, 0
	s_mov_b64 s[70:71], exec
	s_mov_b64 exec, s[76:77]
	global_load_dwordx4 v[128:131], v2, s[58:59] offset:-512 nt
	s_mov_b64 exec, s[70:71]
	v_mov_b32_e32 v132, 0
	v_mov_b32_e32 v133, 0
	v_mov_b32_e32 v134, 0
	v_mov_b32_e32 v135, 0
	s_mov_b64 s[70:71], exec
	s_mov_b64 exec, s[76:77]
	global_load_dwordx4 v[132:135], v2, s[60:61] offset:-512 nt
	s_mov_b64 exec, s[70:71]
	v_mov_b32_e32 v136, 0
	v_mov_b32_e32 v137, 0
	v_mov_b32_e32 v138, 0
	v_mov_b32_e32 v139, 0
	s_mov_b64 s[70:71], exec
	s_mov_b64 exec, s[76:77]
	global_load_dwordx4 v[136:139], v2, s[62:63] offset:-512 nt
	s_mov_b64 exec, s[70:71]
	v_mov_b32_e32 v140, 0
	v_mov_b32_e32 v141, 0
	v_mov_b32_e32 v142, 0
	v_mov_b32_e32 v143, 0
	s_mov_b64 s[70:71], exec
	s_mov_b64 exec, s[76:77]
	global_load_dwordx4 v[140:143], v2, s[64:65] offset:-512 nt
	s_mov_b64 exec, s[70:71]
	v_mov_b32_e32 v144, 0
	v_mov_b32_e32 v145, 0
	v_mov_b32_e32 v146, 0
	v_mov_b32_e32 v147, 0
	s_mov_b64 s[70:71], exec
	s_mov_b64 exec, s[76:77]
	global_load_dwordx4 v[144:147], v2, s[66:67] offset:-512 nt
	s_mov_b64 exec, s[70:71]
	global_load_dwordx4 v[8:11], v2, s[52:53] nt
	global_load_dwordx4 v[12:15], v2, s[54:55] nt
	global_load_dwordx4 v[16:19], v2, s[56:57] nt
	global_load_dwordx4 v[20:23], v2, s[58:59] nt
	global_load_dwordx4 v[24:27], v2, s[60:61] nt
	global_load_dwordx4 v[28:31], v2, s[62:63] nt
	global_load_dwordx4 v[32:35], v2, s[64:65] nt
	global_load_dwordx4 v[36:39], v2, s[66:67] nt
	global_load_dwordx4 v[40:43], v2, s[52:53] offset:512 nt
	global_load_dwordx4 v[44:47], v2, s[54:55] offset:512 nt
	global_load_dwordx4 v[48:51], v2, s[56:57] offset:512 nt
	global_load_dwordx4 v[52:55], v2, s[58:59] offset:512 nt
	global_load_dwordx4 v[56:59], v2, s[60:61] offset:512 nt
	global_load_dwordx4 v[60:63], v2, s[62:63] offset:512 nt
	global_load_dwordx4 v[64:67], v2, s[64:65] offset:512 nt
	global_load_dwordx4 v[68:71], v2, s[66:67] offset:512 nt
	global_load_dwordx4 v[72:75], v2, s[52:53] offset:1024 nt
	global_load_dwordx4 v[76:79], v2, s[54:55] offset:1024 nt
	global_load_dwordx4 v[80:83], v2, s[56:57] offset:1024 nt
	global_load_dwordx4 v[84:87], v2, s[58:59] offset:1024 nt
	global_load_dwordx4 v[88:91], v2, s[60:61] offset:1024 nt
	global_load_dwordx4 v[92:95], v2, s[62:63] offset:1024 nt
	global_load_dwordx4 v[96:99], v2, s[64:65] offset:1024 nt
	global_load_dwordx4 v[100:103], v2, s[66:67] offset:1024 nt
	s_waitcnt vmcnt(31)
	v_cvt_pk_f16_f32 v4, v116, v117
	v_cvt_pk_f16_f32 v5, v118, v119
	s_mov_b64 s[70:71], exec
	s_mov_b64 exec, s[76:77]
	ds_write_b64 v112, v[4:5]
	s_mov_b64 exec, s[70:71]
	s_waitcnt vmcnt(30)
	v_cvt_pk_f16_f32 v4, v120, v121
	v_cvt_pk_f16_f32 v5, v122, v123
	s_mov_b64 s[70:71], exec
	s_mov_b64 exec, s[76:77]
	ds_write_b64 v112, v[4:5] offset:2176
	s_mov_b64 exec, s[70:71]
	s_waitcnt vmcnt(29)
	v_cvt_pk_f16_f32 v4, v124, v125
	v_cvt_pk_f16_f32 v5, v126, v127
	s_mov_b64 s[70:71], exec
	s_mov_b64 exec, s[76:77]
	ds_write_b64 v112, v[4:5] offset:4352
	s_mov_b64 exec, s[70:71]
	s_waitcnt vmcnt(28)
	v_cvt_pk_f16_f32 v4, v128, v129
	v_cvt_pk_f16_f32 v5, v130, v131
	s_mov_b64 s[70:71], exec
	s_mov_b64 exec, s[76:77]
	ds_write_b64 v112, v[4:5] offset:6528
	s_mov_b64 exec, s[70:71]
	s_waitcnt vmcnt(27)
	v_cvt_pk_f16_f32 v4, v132, v133
	v_cvt_pk_f16_f32 v5, v134, v135
	s_mov_b64 s[70:71], exec
	s_mov_b64 exec, s[76:77]
	ds_write_b64 v112, v[4:5] offset:8704
	s_mov_b64 exec, s[70:71]
	s_waitcnt vmcnt(26)
	v_cvt_pk_f16_f32 v4, v136, v137
	v_cvt_pk_f16_f32 v5, v138, v139
	s_mov_b64 s[70:71], exec
	s_mov_b64 exec, s[76:77]
	ds_write_b64 v112, v[4:5] offset:10880
	s_mov_b64 exec, s[70:71]
	s_waitcnt vmcnt(25)
	v_cvt_pk_f16_f32 v4, v140, v141
	v_cvt_pk_f16_f32 v5, v142, v143
	s_mov_b64 s[70:71], exec
	s_mov_b64 exec, s[76:77]
	ds_write_b64 v112, v[4:5] offset:13056
	s_mov_b64 exec, s[70:71]
	s_waitcnt vmcnt(24)
	v_cvt_pk_f16_f32 v4, v144, v145
	v_cvt_pk_f16_f32 v5, v146, v147
	s_mov_b64 s[70:71], exec
	s_mov_b64 exec, s[76:77]
	ds_write_b64 v112, v[4:5] offset:15232
	s_mov_b64 exec, s[70:71]
	s_waitcnt vmcnt(23)
	v_cvt_pk_f16_f32 v4, v8, v9
	v_cvt_pk_f16_f32 v5, v10, v11
	ds_write_b64 v110, v[4:5]
	global_load_dwordx4 v[8:11], v2, s[52:53] offset:1536 nt
	s_waitcnt vmcnt(23)
	v_cvt_pk_f16_f32 v4, v12, v13
	v_cvt_pk_f16_f32 v5, v14, v15
	ds_write_b64 v110, v[4:5] offset:2176
	global_load_dwordx4 v[12:15], v2, s[54:55] offset:1536 nt
	s_waitcnt vmcnt(23)
	v_cvt_pk_f16_f32 v4, v16, v17
	v_cvt_pk_f16_f32 v5, v18, v19
	ds_write_b64 v110, v[4:5] offset:4352
	global_load_dwordx4 v[16:19], v2, s[56:57] offset:1536 nt
	s_waitcnt vmcnt(23)
	v_cvt_pk_f16_f32 v4, v20, v21
	v_cvt_pk_f16_f32 v5, v22, v23
	ds_write_b64 v110, v[4:5] offset:6528
	global_load_dwordx4 v[20:23], v2, s[58:59] offset:1536 nt
	s_waitcnt vmcnt(23)
	v_cvt_pk_f16_f32 v4, v24, v25
	v_cvt_pk_f16_f32 v5, v26, v27
	ds_write_b64 v110, v[4:5] offset:8704
	global_load_dwordx4 v[24:27], v2, s[60:61] offset:1536 nt
	s_waitcnt vmcnt(23)
	v_cvt_pk_f16_f32 v4, v28, v29
	v_cvt_pk_f16_f32 v5, v30, v31
	ds_write_b64 v110, v[4:5] offset:10880
	global_load_dwordx4 v[28:31], v2, s[62:63] offset:1536 nt
	s_waitcnt vmcnt(23)
	v_cvt_pk_f16_f32 v4, v32, v33
	v_cvt_pk_f16_f32 v5, v34, v35
	ds_write_b64 v110, v[4:5] offset:13056
	global_load_dwordx4 v[32:35], v2, s[64:65] offset:1536 nt
	s_waitcnt vmcnt(23)
	v_cvt_pk_f16_f32 v4, v36, v37
	v_cvt_pk_f16_f32 v5, v38, v39
	ds_write_b64 v110, v[4:5] offset:15232
	global_load_dwordx4 v[36:39], v2, s[66:67] offset:1536 nt
	s_waitcnt lgkmcnt(0)
	s_barrier
	s_waitcnt vmcnt(23)
	v_cvt_pk_f16_f32 v4, v40, v41
	v_cvt_pk_f16_f32 v5, v42, v43
	ds_write_b64 v111, v[4:5]
	global_load_dwordx4 v[40:43], v2, s[52:53] offset:2048 nt
	s_waitcnt vmcnt(23)
	v_cvt_pk_f16_f32 v4, v44, v45
	v_cvt_pk_f16_f32 v5, v46, v47
	ds_write_b64 v111, v[4:5] offset:2176
	global_load_dwordx4 v[44:47], v2, s[54:55] offset:2048 nt
	s_waitcnt vmcnt(23)
	v_cvt_pk_f16_f32 v4, v48, v49
	v_cvt_pk_f16_f32 v5, v50, v51
	ds_write_b64 v111, v[4:5] offset:4352
	global_load_dwordx4 v[48:51], v2, s[56:57] offset:2048 nt
	s_waitcnt vmcnt(23)
	v_cvt_pk_f16_f32 v4, v52, v53
	v_cvt_pk_f16_f32 v5, v54, v55
	ds_write_b64 v111, v[4:5] offset:6528
	global_load_dwordx4 v[52:55], v2, s[58:59] offset:2048 nt
	s_waitcnt vmcnt(23)
	v_cvt_pk_f16_f32 v4, v56, v57
	v_cvt_pk_f16_f32 v5, v58, v59
	ds_write_b64 v111, v[4:5] offset:8704
	global_load_dwordx4 v[56:59], v2, s[60:61] offset:2048 nt
	s_waitcnt vmcnt(23)
	v_cvt_pk_f16_f32 v4, v60, v61
	v_cvt_pk_f16_f32 v5, v62, v63
	ds_write_b64 v111, v[4:5] offset:10880
	global_load_dwordx4 v[60:63], v2, s[62:63] offset:2048 nt
	s_waitcnt vmcnt(23)
	v_cvt_pk_f16_f32 v4, v64, v65
	v_cvt_pk_f16_f32 v5, v66, v67
	ds_write_b64 v111, v[4:5] offset:13056
	global_load_dwordx4 v[64:67], v2, s[64:65] offset:2048 nt
	s_waitcnt vmcnt(23)
	v_cvt_pk_f16_f32 v4, v68, v69
	v_cvt_pk_f16_f32 v5, v70, v71
	ds_write_b64 v111, v[4:5] offset:15232
	global_load_dwordx4 v[68:71], v2, s[66:67] offset:2048 nt
	s_waitcnt lgkmcnt(0)
	s_barrier
	s_waitcnt vmcnt(23)
	v_cvt_pk_f16_f32 v4, v72, v73
	v_cvt_pk_f16_f32 v5, v74, v75
	ds_write_b64 v112, v[4:5]
	global_load_dwordx4 v[72:75], v2, s[52:53] offset:2560 nt
	s_waitcnt vmcnt(23)
	v_cvt_pk_f16_f32 v4, v76, v77
	v_cvt_pk_f16_f32 v5, v78, v79
	ds_write_b64 v112, v[4:5] offset:2176
	global_load_dwordx4 v[76:79], v2, s[54:55] offset:2560 nt
	s_waitcnt vmcnt(23)
	v_cvt_pk_f16_f32 v4, v80, v81
	v_cvt_pk_f16_f32 v5, v82, v83
	ds_write_b64 v112, v[4:5] offset:4352
	global_load_dwordx4 v[80:83], v2, s[56:57] offset:2560 nt
	s_waitcnt vmcnt(23)
	v_cvt_pk_f16_f32 v4, v84, v85
	v_cvt_pk_f16_f32 v5, v86, v87
	ds_write_b64 v112, v[4:5] offset:6528
	global_load_dwordx4 v[84:87], v2, s[58:59] offset:2560 nt
	s_waitcnt vmcnt(23)
	v_cvt_pk_f16_f32 v4, v88, v89
	v_cvt_pk_f16_f32 v5, v90, v91
	ds_write_b64 v112, v[4:5] offset:8704
	global_load_dwordx4 v[88:91], v2, s[60:61] offset:2560 nt
	s_waitcnt vmcnt(23)
	v_cvt_pk_f16_f32 v4, v92, v93
	v_cvt_pk_f16_f32 v5, v94, v95
	ds_write_b64 v112, v[4:5] offset:10880
	global_load_dwordx4 v[92:95], v2, s[62:63] offset:2560 nt
	s_waitcnt vmcnt(23)
	v_cvt_pk_f16_f32 v4, v96, v97
	v_cvt_pk_f16_f32 v5, v98, v99
	ds_write_b64 v112, v[4:5] offset:13056
	global_load_dwordx4 v[96:99], v2, s[64:65] offset:2560 nt
	s_waitcnt vmcnt(23)
	v_cvt_pk_f16_f32 v4, v100, v101
	v_cvt_pk_f16_f32 v5, v102, v103
	ds_write_b64 v112, v[4:5] offset:15232
	global_load_dwordx4 v[100:103], v2, s[66:67] offset:2560 nt
	s_waitcnt lgkmcnt(0)
	s_barrier
	s_waitcnt vmcnt(23)
	v_cvt_pk_f16_f32 v4, v8, v9
	v_cvt_pk_f16_f32 v5, v10, v11
	ds_write_b64 v110, v[4:5]
	global_load_dwordx4 v[8:11], v2, s[52:53] offset:3072 nt
	s_waitcnt vmcnt(23)
	v_cvt_pk_f16_f32 v4, v12, v13
	v_cvt_pk_f16_f32 v5, v14, v15
	ds_write_b64 v110, v[4:5] offset:2176
	global_load_dwordx4 v[12:15], v2, s[54:55] offset:3072 nt
	s_waitcnt vmcnt(23)
	v_cvt_pk_f16_f32 v4, v16, v17
	v_cvt_pk_f16_f32 v5, v18, v19
	ds_write_b64 v110, v[4:5] offset:4352
	global_load_dwordx4 v[16:19], v2, s[56:57] offset:3072 nt
	s_waitcnt vmcnt(23)
	v_cvt_pk_f16_f32 v4, v20, v21
	v_cvt_pk_f16_f32 v5, v22, v23
	ds_write_b64 v110, v[4:5] offset:6528
	global_load_dwordx4 v[20:23], v2, s[58:59] offset:3072 nt
	s_waitcnt vmcnt(23)
	v_cvt_pk_f16_f32 v4, v24, v25
	v_cvt_pk_f16_f32 v5, v26, v27
	ds_write_b64 v110, v[4:5] offset:8704
	global_load_dwordx4 v[24:27], v2, s[60:61] offset:3072 nt
	s_waitcnt vmcnt(23)
	v_cvt_pk_f16_f32 v4, v28, v29
	v_cvt_pk_f16_f32 v5, v30, v31
	ds_write_b64 v110, v[4:5] offset:10880
	global_load_dwordx4 v[28:31], v2, s[62:63] offset:3072 nt
	s_waitcnt vmcnt(23)
	v_cvt_pk_f16_f32 v4, v32, v33
	v_cvt_pk_f16_f32 v5, v34, v35
	ds_write_b64 v110, v[4:5] offset:13056
	global_load_dwordx4 v[32:35], v2, s[64:65] offset:3072 nt
	s_waitcnt vmcnt(23)
	v_cvt_pk_f16_f32 v4, v36, v37
	v_cvt_pk_f16_f32 v5, v38, v39
	ds_write_b64 v110, v[4:5] offset:15232
	global_load_dwordx4 v[36:39], v2, s[66:67] offset:3072 nt
	s_waitcnt lgkmcnt(0)
	s_barrier
	s_waitcnt vmcnt(23)
	v_cvt_pk_f16_f32 v4, v40, v41
	v_cvt_pk_f16_f32 v5, v42, v43
	ds_write_b64 v111, v[4:5]
	global_load_dwordx4 v[40:43], v2, s[52:53] offset:3584 nt
	s_waitcnt vmcnt(23)
	v_cvt_pk_f16_f32 v4, v44, v45
	v_cvt_pk_f16_f32 v5, v46, v47
	ds_write_b64 v111, v[4:5] offset:2176
	global_load_dwordx4 v[44:47], v2, s[54:55] offset:3584 nt
	s_waitcnt vmcnt(23)
	v_cvt_pk_f16_f32 v4, v48, v49
	v_cvt_pk_f16_f32 v5, v50, v51
	ds_write_b64 v111, v[4:5] offset:4352
	global_load_dwordx4 v[48:51], v2, s[56:57] offset:3584 nt
	s_waitcnt vmcnt(23)
	v_cvt_pk_f16_f32 v4, v52, v53
	v_cvt_pk_f16_f32 v5, v54, v55
	ds_write_b64 v111, v[4:5] offset:6528
	global_load_dwordx4 v[52:55], v2, s[58:59] offset:3584 nt
	s_waitcnt vmcnt(23)
	v_cvt_pk_f16_f32 v4, v56, v57
	v_cvt_pk_f16_f32 v5, v58, v59
	ds_write_b64 v111, v[4:5] offset:8704
	global_load_dwordx4 v[56:59], v2, s[60:61] offset:3584 nt
	s_waitcnt vmcnt(23)
	v_cvt_pk_f16_f32 v4, v60, v61
	v_cvt_pk_f16_f32 v5, v62, v63
	ds_write_b64 v111, v[4:5] offset:10880
	global_load_dwordx4 v[60:63], v2, s[62:63] offset:3584 nt
	s_waitcnt vmcnt(23)
	v_cvt_pk_f16_f32 v4, v64, v65
	v_cvt_pk_f16_f32 v5, v66, v67
	ds_write_b64 v111, v[4:5] offset:13056
	global_load_dwordx4 v[64:67], v2, s[64:65] offset:3584 nt
	s_waitcnt vmcnt(23)
	v_cvt_pk_f16_f32 v4, v68, v69
	v_cvt_pk_f16_f32 v5, v70, v71
	ds_write_b64 v111, v[4:5] offset:15232
	global_load_dwordx4 v[68:71], v2, s[66:67] offset:3584 nt
	s_waitcnt lgkmcnt(0)
	s_barrier
	s_waitcnt vmcnt(23)
	v_cvt_pk_f16_f32 v4, v72, v73
	v_cvt_pk_f16_f32 v5, v74, v75
	ds_write_b64 v112, v[4:5]
	v_add_u32_e32 v2, 0x1000, v2
	global_load_dwordx4 v[72:75], v2, s[52:53] nt
	s_waitcnt vmcnt(23)
	v_cvt_pk_f16_f32 v4, v76, v77
	v_cvt_pk_f16_f32 v5, v78, v79
	ds_write_b64 v112, v[4:5] offset:2176
	global_load_dwordx4 v[76:79], v2, s[54:55] nt
	s_waitcnt vmcnt(23)
	v_cvt_pk_f16_f32 v4, v80, v81
	v_cvt_pk_f16_f32 v5, v82, v83
	ds_write_b64 v112, v[4:5] offset:4352
	global_load_dwordx4 v[80:83], v2, s[56:57] nt
	s_waitcnt vmcnt(23)
	v_cvt_pk_f16_f32 v4, v84, v85
	v_cvt_pk_f16_f32 v5, v86, v87
	ds_write_b64 v112, v[4:5] offset:6528
	global_load_dwordx4 v[84:87], v2, s[58:59] nt
	s_waitcnt vmcnt(23)
	v_cvt_pk_f16_f32 v4, v88, v89
	v_cvt_pk_f16_f32 v5, v90, v91
	ds_write_b64 v112, v[4:5] offset:8704
	global_load_dwordx4 v[88:91], v2, s[60:61] nt
	s_waitcnt vmcnt(23)
	v_cvt_pk_f16_f32 v4, v92, v93
	v_cvt_pk_f16_f32 v5, v94, v95
	ds_write_b64 v112, v[4:5] offset:10880
	global_load_dwordx4 v[92:95], v2, s[62:63] nt
	s_waitcnt vmcnt(23)
	v_cvt_pk_f16_f32 v4, v96, v97
	v_cvt_pk_f16_f32 v5, v98, v99
	ds_write_b64 v112, v[4:5] offset:13056
	global_load_dwordx4 v[96:99], v2, s[64:65] nt
	s_waitcnt vmcnt(23)
	v_cvt_pk_f16_f32 v4, v100, v101
	v_cvt_pk_f16_f32 v5, v102, v103
	ds_write_b64 v112, v[4:5] offset:15232
	global_load_dwordx4 v[100:103], v2, s[66:67] nt
	s_waitcnt lgkmcnt(0)
	s_barrier
	s_waitcnt vmcnt(23)
	v_cvt_pk_f16_f32 v4, v8, v9
	v_cvt_pk_f16_f32 v5, v10, v11
	ds_write_b64 v110, v[4:5]
	global_load_dwordx4 v[8:11], v2, s[52:53] offset:512 nt
	s_waitcnt vmcnt(23)
	v_cvt_pk_f16_f32 v4, v12, v13
	v_cvt_pk_f16_f32 v5, v14, v15
	ds_write_b64 v110, v[4:5] offset:2176
	global_load_dwordx4 v[12:15], v2, s[54:55] offset:512 nt
	s_waitcnt vmcnt(23)
	v_cvt_pk_f16_f32 v4, v16, v17
	v_cvt_pk_f16_f32 v5, v18, v19
	ds_write_b64 v110, v[4:5] offset:4352
	global_load_dwordx4 v[16:19], v2, s[56:57] offset:512 nt
	s_waitcnt vmcnt(23)
	v_cvt_pk_f16_f32 v4, v20, v21
	v_cvt_pk_f16_f32 v5, v22, v23
	ds_write_b64 v110, v[4:5] offset:6528
	global_load_dwordx4 v[20:23], v2, s[58:59] offset:512 nt
	s_waitcnt vmcnt(23)
	v_cvt_pk_f16_f32 v4, v24, v25
	v_cvt_pk_f16_f32 v5, v26, v27
	ds_write_b64 v110, v[4:5] offset:8704
	global_load_dwordx4 v[24:27], v2, s[60:61] offset:512 nt
	s_waitcnt vmcnt(23)
	v_cvt_pk_f16_f32 v4, v28, v29
	v_cvt_pk_f16_f32 v5, v30, v31
	ds_write_b64 v110, v[4:5] offset:10880
	global_load_dwordx4 v[28:31], v2, s[62:63] offset:512 nt
	s_waitcnt vmcnt(23)
	v_cvt_pk_f16_f32 v4, v32, v33
	v_cvt_pk_f16_f32 v5, v34, v35
	ds_write_b64 v110, v[4:5] offset:13056
	global_load_dwordx4 v[32:35], v2, s[64:65] offset:512 nt
	s_waitcnt vmcnt(23)
	v_cvt_pk_f16_f32 v4, v36, v37
	v_cvt_pk_f16_f32 v5, v38, v39
	ds_write_b64 v110, v[4:5] offset:15232
	global_load_dwordx4 v[36:39], v2, s[66:67] offset:512 nt
	s_waitcnt lgkmcnt(0)
	s_barrier
	s_waitcnt vmcnt(23)
	v_cvt_pk_f16_f32 v4, v40, v41
	v_cvt_pk_f16_f32 v5, v42, v43
	ds_write_b64 v111, v[4:5]
	global_load_dwordx4 v[40:43], v2, s[52:53] offset:1024 nt
	s_waitcnt vmcnt(23)
	v_cvt_pk_f16_f32 v4, v44, v45
	v_cvt_pk_f16_f32 v5, v46, v47
	ds_write_b64 v111, v[4:5] offset:2176
	global_load_dwordx4 v[44:47], v2, s[54:55] offset:1024 nt
	s_waitcnt vmcnt(23)
	v_cvt_pk_f16_f32 v4, v48, v49
	v_cvt_pk_f16_f32 v5, v50, v51
	ds_write_b64 v111, v[4:5] offset:4352
	global_load_dwordx4 v[48:51], v2, s[56:57] offset:1024 nt
	s_waitcnt vmcnt(23)
	v_cvt_pk_f16_f32 v4, v52, v53
	v_cvt_pk_f16_f32 v5, v54, v55
	ds_write_b64 v111, v[4:5] offset:6528
	global_load_dwordx4 v[52:55], v2, s[58:59] offset:1024 nt
	s_waitcnt vmcnt(23)
	v_cvt_pk_f16_f32 v4, v56, v57
	v_cvt_pk_f16_f32 v5, v58, v59
	ds_write_b64 v111, v[4:5] offset:8704
	global_load_dwordx4 v[56:59], v2, s[60:61] offset:1024 nt
	s_waitcnt vmcnt(23)
	v_cvt_pk_f16_f32 v4, v60, v61
	v_cvt_pk_f16_f32 v5, v62, v63
	ds_write_b64 v111, v[4:5] offset:10880
	global_load_dwordx4 v[60:63], v2, s[62:63] offset:1024 nt
	s_waitcnt vmcnt(23)
	v_cvt_pk_f16_f32 v4, v64, v65
	v_cvt_pk_f16_f32 v5, v66, v67
	ds_write_b64 v111, v[4:5] offset:13056
	global_load_dwordx4 v[64:67], v2, s[64:65] offset:1024 nt
	s_waitcnt vmcnt(23)
	v_cvt_pk_f16_f32 v4, v68, v69
	v_cvt_pk_f16_f32 v5, v70, v71
	ds_write_b64 v111, v[4:5] offset:15232
	global_load_dwordx4 v[68:71], v2, s[66:67] offset:1024 nt
	s_waitcnt lgkmcnt(0)
	s_barrier
	s_waitcnt vmcnt(23)
	v_cvt_pk_f16_f32 v4, v72, v73
	v_cvt_pk_f16_f32 v5, v74, v75
	ds_write_b64 v112, v[4:5]
	global_load_dwordx4 v[72:75], v2, s[52:53] offset:1536 nt
	s_waitcnt vmcnt(23)
	v_cvt_pk_f16_f32 v4, v76, v77
	v_cvt_pk_f16_f32 v5, v78, v79
	ds_write_b64 v112, v[4:5] offset:2176
	global_load_dwordx4 v[76:79], v2, s[54:55] offset:1536 nt
	s_waitcnt vmcnt(23)
	v_cvt_pk_f16_f32 v4, v80, v81
	v_cvt_pk_f16_f32 v5, v82, v83
	ds_write_b64 v112, v[4:5] offset:4352
	global_load_dwordx4 v[80:83], v2, s[56:57] offset:1536 nt
	s_waitcnt vmcnt(23)
	v_cvt_pk_f16_f32 v4, v84, v85
	v_cvt_pk_f16_f32 v5, v86, v87
	ds_write_b64 v112, v[4:5] offset:6528
	global_load_dwordx4 v[84:87], v2, s[58:59] offset:1536 nt
	s_waitcnt vmcnt(23)
	v_cvt_pk_f16_f32 v4, v88, v89
	v_cvt_pk_f16_f32 v5, v90, v91
	ds_write_b64 v112, v[4:5] offset:8704
	global_load_dwordx4 v[88:91], v2, s[60:61] offset:1536 nt
	s_waitcnt vmcnt(23)
	v_cvt_pk_f16_f32 v4, v92, v93
	v_cvt_pk_f16_f32 v5, v94, v95
	ds_write_b64 v112, v[4:5] offset:10880
	global_load_dwordx4 v[92:95], v2, s[62:63] offset:1536 nt
	s_waitcnt vmcnt(23)
	v_cvt_pk_f16_f32 v4, v96, v97
	v_cvt_pk_f16_f32 v5, v98, v99
	ds_write_b64 v112, v[4:5] offset:13056
	global_load_dwordx4 v[96:99], v2, s[64:65] offset:1536 nt
	s_waitcnt vmcnt(23)
	v_cvt_pk_f16_f32 v4, v100, v101
	v_cvt_pk_f16_f32 v5, v102, v103
	ds_write_b64 v112, v[4:5] offset:15232
	global_load_dwordx4 v[100:103], v2, s[66:67] offset:1536 nt
	s_waitcnt lgkmcnt(0)
	s_barrier
	s_waitcnt vmcnt(23)
	v_cvt_pk_f16_f32 v4, v8, v9
	v_cvt_pk_f16_f32 v5, v10, v11
	ds_write_b64 v110, v[4:5]
	global_load_dwordx4 v[8:11], v2, s[52:53] offset:2048 nt
	s_waitcnt vmcnt(23)
	v_cvt_pk_f16_f32 v4, v12, v13
	v_cvt_pk_f16_f32 v5, v14, v15
	ds_write_b64 v110, v[4:5] offset:2176
	global_load_dwordx4 v[12:15], v2, s[54:55] offset:2048 nt
	s_waitcnt vmcnt(23)
	v_cvt_pk_f16_f32 v4, v16, v17
	v_cvt_pk_f16_f32 v5, v18, v19
	ds_write_b64 v110, v[4:5] offset:4352
	global_load_dwordx4 v[16:19], v2, s[56:57] offset:2048 nt
	s_waitcnt vmcnt(23)
	v_cvt_pk_f16_f32 v4, v20, v21
	v_cvt_pk_f16_f32 v5, v22, v23
	ds_write_b64 v110, v[4:5] offset:6528
	global_load_dwordx4 v[20:23], v2, s[58:59] offset:2048 nt
	s_waitcnt vmcnt(23)
	v_cvt_pk_f16_f32 v4, v24, v25
	v_cvt_pk_f16_f32 v5, v26, v27
	ds_write_b64 v110, v[4:5] offset:8704
	global_load_dwordx4 v[24:27], v2, s[60:61] offset:2048 nt
	s_waitcnt vmcnt(23)
	v_cvt_pk_f16_f32 v4, v28, v29
	v_cvt_pk_f16_f32 v5, v30, v31
	ds_write_b64 v110, v[4:5] offset:10880
	global_load_dwordx4 v[28:31], v2, s[62:63] offset:2048 nt
	s_waitcnt vmcnt(23)
	v_cvt_pk_f16_f32 v4, v32, v33
	v_cvt_pk_f16_f32 v5, v34, v35
	ds_write_b64 v110, v[4:5] offset:13056
	global_load_dwordx4 v[32:35], v2, s[64:65] offset:2048 nt
	s_waitcnt vmcnt(23)
	v_cvt_pk_f16_f32 v4, v36, v37
	v_cvt_pk_f16_f32 v5, v38, v39
	ds_write_b64 v110, v[4:5] offset:15232
	global_load_dwordx4 v[36:39], v2, s[66:67] offset:2048 nt
	s_waitcnt lgkmcnt(0)
	s_barrier
	s_waitcnt vmcnt(23)
	v_cvt_pk_f16_f32 v4, v40, v41
	v_cvt_pk_f16_f32 v5, v42, v43
	ds_write_b64 v111, v[4:5]
	global_load_dwordx4 v[40:43], v2, s[52:53] offset:2560 nt
	s_waitcnt vmcnt(23)
	v_cvt_pk_f16_f32 v4, v44, v45
	v_cvt_pk_f16_f32 v5, v46, v47
	ds_write_b64 v111, v[4:5] offset:2176
	global_load_dwordx4 v[44:47], v2, s[54:55] offset:2560 nt
	s_waitcnt vmcnt(23)
	v_cvt_pk_f16_f32 v4, v48, v49
	v_cvt_pk_f16_f32 v5, v50, v51
	ds_write_b64 v111, v[4:5] offset:4352
	global_load_dwordx4 v[48:51], v2, s[56:57] offset:2560 nt
	s_waitcnt vmcnt(23)
	v_cvt_pk_f16_f32 v4, v52, v53
	v_cvt_pk_f16_f32 v5, v54, v55
	ds_write_b64 v111, v[4:5] offset:6528
	global_load_dwordx4 v[52:55], v2, s[58:59] offset:2560 nt
	s_waitcnt vmcnt(23)
	v_cvt_pk_f16_f32 v4, v56, v57
	v_cvt_pk_f16_f32 v5, v58, v59
	ds_write_b64 v111, v[4:5] offset:8704
	global_load_dwordx4 v[56:59], v2, s[60:61] offset:2560 nt
	s_waitcnt vmcnt(23)
	v_cvt_pk_f16_f32 v4, v60, v61
	v_cvt_pk_f16_f32 v5, v62, v63
	ds_write_b64 v111, v[4:5] offset:10880
	global_load_dwordx4 v[60:63], v2, s[62:63] offset:2560 nt
	s_waitcnt vmcnt(23)
	v_cvt_pk_f16_f32 v4, v64, v65
	v_cvt_pk_f16_f32 v5, v66, v67
	ds_write_b64 v111, v[4:5] offset:13056
	global_load_dwordx4 v[64:67], v2, s[64:65] offset:2560 nt
	s_waitcnt vmcnt(23)
	v_cvt_pk_f16_f32 v4, v68, v69
	v_cvt_pk_f16_f32 v5, v70, v71
	ds_write_b64 v111, v[4:5] offset:15232
	global_load_dwordx4 v[68:71], v2, s[66:67] offset:2560 nt
	s_waitcnt lgkmcnt(0)
	s_barrier
	s_waitcnt vmcnt(23)
	v_cvt_pk_f16_f32 v4, v72, v73
	v_cvt_pk_f16_f32 v5, v74, v75
	ds_write_b64 v112, v[4:5]
	global_load_dwordx4 v[72:75], v2, s[52:53] offset:3072 nt
	s_waitcnt vmcnt(23)
	v_cvt_pk_f16_f32 v4, v76, v77
	v_cvt_pk_f16_f32 v5, v78, v79
	ds_write_b64 v112, v[4:5] offset:2176
	global_load_dwordx4 v[76:79], v2, s[54:55] offset:3072 nt
	s_waitcnt vmcnt(23)
	v_cvt_pk_f16_f32 v4, v80, v81
	v_cvt_pk_f16_f32 v5, v82, v83
	ds_write_b64 v112, v[4:5] offset:4352
	global_load_dwordx4 v[80:83], v2, s[56:57] offset:3072 nt
	s_waitcnt vmcnt(23)
	v_cvt_pk_f16_f32 v4, v84, v85
	v_cvt_pk_f16_f32 v5, v86, v87
	ds_write_b64 v112, v[4:5] offset:6528
	global_load_dwordx4 v[84:87], v2, s[58:59] offset:3072 nt
	s_waitcnt vmcnt(23)
	v_cvt_pk_f16_f32 v4, v88, v89
	v_cvt_pk_f16_f32 v5, v90, v91
	ds_write_b64 v112, v[4:5] offset:8704
	global_load_dwordx4 v[88:91], v2, s[60:61] offset:3072 nt
	s_waitcnt vmcnt(23)
	v_cvt_pk_f16_f32 v4, v92, v93
	v_cvt_pk_f16_f32 v5, v94, v95
	ds_write_b64 v112, v[4:5] offset:10880
	global_load_dwordx4 v[92:95], v2, s[62:63] offset:3072 nt
	s_waitcnt vmcnt(23)
	v_cvt_pk_f16_f32 v4, v96, v97
	v_cvt_pk_f16_f32 v5, v98, v99
	ds_write_b64 v112, v[4:5] offset:13056
	global_load_dwordx4 v[96:99], v2, s[64:65] offset:3072 nt
	s_waitcnt vmcnt(23)
	v_cvt_pk_f16_f32 v4, v100, v101
	v_cvt_pk_f16_f32 v5, v102, v103
	ds_write_b64 v112, v[4:5] offset:15232
	global_load_dwordx4 v[100:103], v2, s[66:67] offset:3072 nt
	s_waitcnt lgkmcnt(0)
	s_barrier
	s_waitcnt vmcnt(23)
	v_cvt_pk_f16_f32 v4, v8, v9
	v_cvt_pk_f16_f32 v5, v10, v11
	ds_write_b64 v110, v[4:5]
	global_load_dwordx4 v[8:11], v2, s[52:53] offset:3584 nt
	s_waitcnt vmcnt(23)
	v_cvt_pk_f16_f32 v4, v12, v13
	v_cvt_pk_f16_f32 v5, v14, v15
	ds_write_b64 v110, v[4:5] offset:2176
	global_load_dwordx4 v[12:15], v2, s[54:55] offset:3584 nt
	s_waitcnt vmcnt(23)
	v_cvt_pk_f16_f32 v4, v16, v17
	v_cvt_pk_f16_f32 v5, v18, v19
	ds_write_b64 v110, v[4:5] offset:4352
	global_load_dwordx4 v[16:19], v2, s[56:57] offset:3584 nt
	s_waitcnt vmcnt(23)
	v_cvt_pk_f16_f32 v4, v20, v21
	v_cvt_pk_f16_f32 v5, v22, v23
	ds_write_b64 v110, v[4:5] offset:6528
	global_load_dwordx4 v[20:23], v2, s[58:59] offset:3584 nt
	s_waitcnt vmcnt(23)
	v_cvt_pk_f16_f32 v4, v24, v25
	v_cvt_pk_f16_f32 v5, v26, v27
	ds_write_b64 v110, v[4:5] offset:8704
	global_load_dwordx4 v[24:27], v2, s[60:61] offset:3584 nt
	s_waitcnt vmcnt(23)
	v_cvt_pk_f16_f32 v4, v28, v29
	v_cvt_pk_f16_f32 v5, v30, v31
	ds_write_b64 v110, v[4:5] offset:10880
	global_load_dwordx4 v[28:31], v2, s[62:63] offset:3584 nt
	s_waitcnt vmcnt(23)
	v_cvt_pk_f16_f32 v4, v32, v33
	v_cvt_pk_f16_f32 v5, v34, v35
	ds_write_b64 v110, v[4:5] offset:13056
	global_load_dwordx4 v[32:35], v2, s[64:65] offset:3584 nt
	s_waitcnt vmcnt(23)
	v_cvt_pk_f16_f32 v4, v36, v37
	v_cvt_pk_f16_f32 v5, v38, v39
	ds_write_b64 v110, v[4:5] offset:15232
	global_load_dwordx4 v[36:39], v2, s[66:67] offset:3584 nt
	s_waitcnt lgkmcnt(0)
	s_barrier
	s_waitcnt vmcnt(23)
	v_cvt_pk_f16_f32 v4, v40, v41
	v_cvt_pk_f16_f32 v5, v42, v43
	ds_write_b64 v111, v[4:5]
	v_add_u32_e32 v2, 0x1000, v2
	global_load_dwordx4 v[40:43], v2, s[52:53] nt
	s_waitcnt vmcnt(23)
	v_cvt_pk_f16_f32 v4, v44, v45
	v_cvt_pk_f16_f32 v5, v46, v47
	ds_write_b64 v111, v[4:5] offset:2176
	global_load_dwordx4 v[44:47], v2, s[54:55] nt
	s_waitcnt vmcnt(23)
	v_cvt_pk_f16_f32 v4, v48, v49
	v_cvt_pk_f16_f32 v5, v50, v51
	ds_write_b64 v111, v[4:5] offset:4352
	global_load_dwordx4 v[48:51], v2, s[56:57] nt
	s_waitcnt vmcnt(23)
	v_cvt_pk_f16_f32 v4, v52, v53
	v_cvt_pk_f16_f32 v5, v54, v55
	ds_write_b64 v111, v[4:5] offset:6528
	global_load_dwordx4 v[52:55], v2, s[58:59] nt
	s_waitcnt vmcnt(23)
	v_cvt_pk_f16_f32 v4, v56, v57
	v_cvt_pk_f16_f32 v5, v58, v59
	ds_write_b64 v111, v[4:5] offset:8704
	global_load_dwordx4 v[56:59], v2, s[60:61] nt
	s_waitcnt vmcnt(23)
	v_cvt_pk_f16_f32 v4, v60, v61
	v_cvt_pk_f16_f32 v5, v62, v63
	ds_write_b64 v111, v[4:5] offset:10880
	global_load_dwordx4 v[60:63], v2, s[62:63] nt
	s_waitcnt vmcnt(23)
	v_cvt_pk_f16_f32 v4, v64, v65
	v_cvt_pk_f16_f32 v5, v66, v67
	ds_write_b64 v111, v[4:5] offset:13056
	global_load_dwordx4 v[64:67], v2, s[64:65] nt
	s_waitcnt vmcnt(23)
	v_cvt_pk_f16_f32 v4, v68, v69
	v_cvt_pk_f16_f32 v5, v70, v71
	ds_write_b64 v111, v[4:5] offset:15232
	global_load_dwordx4 v[68:71], v2, s[66:67] nt
	s_waitcnt lgkmcnt(0)
	s_barrier
	s_waitcnt vmcnt(23)
	v_cvt_pk_f16_f32 v4, v72, v73
	v_cvt_pk_f16_f32 v5, v74, v75
	ds_write_b64 v112, v[4:5]
	global_load_dwordx4 v[72:75], v2, s[52:53] offset:512 nt
	s_waitcnt vmcnt(23)
	v_cvt_pk_f16_f32 v4, v76, v77
	v_cvt_pk_f16_f32 v5, v78, v79
	ds_write_b64 v112, v[4:5] offset:2176
	global_load_dwordx4 v[76:79], v2, s[54:55] offset:512 nt
	s_waitcnt vmcnt(23)
	v_cvt_pk_f16_f32 v4, v80, v81
	v_cvt_pk_f16_f32 v5, v82, v83
	ds_write_b64 v112, v[4:5] offset:4352
	global_load_dwordx4 v[80:83], v2, s[56:57] offset:512 nt
	s_waitcnt vmcnt(23)
	v_cvt_pk_f16_f32 v4, v84, v85
	v_cvt_pk_f16_f32 v5, v86, v87
	ds_write_b64 v112, v[4:5] offset:6528
	global_load_dwordx4 v[84:87], v2, s[58:59] offset:512 nt
	s_waitcnt vmcnt(23)
	v_cvt_pk_f16_f32 v4, v88, v89
	v_cvt_pk_f16_f32 v5, v90, v91
	ds_write_b64 v112, v[4:5] offset:8704
	global_load_dwordx4 v[88:91], v2, s[60:61] offset:512 nt
	s_waitcnt vmcnt(23)
	v_cvt_pk_f16_f32 v4, v92, v93
	v_cvt_pk_f16_f32 v5, v94, v95
	ds_write_b64 v112, v[4:5] offset:10880
	global_load_dwordx4 v[92:95], v2, s[62:63] offset:512 nt
	s_waitcnt vmcnt(23)
	v_cvt_pk_f16_f32 v4, v96, v97
	v_cvt_pk_f16_f32 v5, v98, v99
	ds_write_b64 v112, v[4:5] offset:13056
	global_load_dwordx4 v[96:99], v2, s[64:65] offset:512 nt
	s_waitcnt vmcnt(23)
	v_cvt_pk_f16_f32 v4, v100, v101
	v_cvt_pk_f16_f32 v5, v102, v103
	ds_write_b64 v112, v[4:5] offset:15232
	global_load_dwordx4 v[100:103], v2, s[66:67] offset:512 nt
	s_waitcnt lgkmcnt(0)
	s_barrier
	s_waitcnt vmcnt(23)
	v_cvt_pk_f16_f32 v4, v8, v9
	v_cvt_pk_f16_f32 v5, v10, v11
	ds_write_b64 v110, v[4:5]
	global_load_dwordx4 v[8:11], v2, s[52:53] offset:1024 nt
	s_waitcnt vmcnt(23)
	v_cvt_pk_f16_f32 v4, v12, v13
	v_cvt_pk_f16_f32 v5, v14, v15
	ds_write_b64 v110, v[4:5] offset:2176
	global_load_dwordx4 v[12:15], v2, s[54:55] offset:1024 nt
	s_waitcnt vmcnt(23)
	v_cvt_pk_f16_f32 v4, v16, v17
	v_cvt_pk_f16_f32 v5, v18, v19
	ds_write_b64 v110, v[4:5] offset:4352
	global_load_dwordx4 v[16:19], v2, s[56:57] offset:1024 nt
	s_waitcnt vmcnt(23)
	v_cvt_pk_f16_f32 v4, v20, v21
	v_cvt_pk_f16_f32 v5, v22, v23
	ds_write_b64 v110, v[4:5] offset:6528
	global_load_dwordx4 v[20:23], v2, s[58:59] offset:1024 nt
	s_waitcnt vmcnt(23)
	v_cvt_pk_f16_f32 v4, v24, v25
	v_cvt_pk_f16_f32 v5, v26, v27
	ds_write_b64 v110, v[4:5] offset:8704
	global_load_dwordx4 v[24:27], v2, s[60:61] offset:1024 nt
	s_waitcnt vmcnt(23)
	v_cvt_pk_f16_f32 v4, v28, v29
	v_cvt_pk_f16_f32 v5, v30, v31
	ds_write_b64 v110, v[4:5] offset:10880
	global_load_dwordx4 v[28:31], v2, s[62:63] offset:1024 nt
	s_waitcnt vmcnt(23)
	v_cvt_pk_f16_f32 v4, v32, v33
	v_cvt_pk_f16_f32 v5, v34, v35
	ds_write_b64 v110, v[4:5] offset:13056
	global_load_dwordx4 v[32:35], v2, s[64:65] offset:1024 nt
	s_waitcnt vmcnt(23)
	v_cvt_pk_f16_f32 v4, v36, v37
	v_cvt_pk_f16_f32 v5, v38, v39
	ds_write_b64 v110, v[4:5] offset:15232
	global_load_dwordx4 v[36:39], v2, s[66:67] offset:1024 nt
	s_waitcnt lgkmcnt(0)
	s_barrier
	s_waitcnt vmcnt(23)
	v_cvt_pk_f16_f32 v4, v40, v41
	v_cvt_pk_f16_f32 v5, v42, v43
	ds_write_b64 v111, v[4:5]
	global_load_dwordx4 v[40:43], v2, s[52:53] offset:1536 nt
	s_waitcnt vmcnt(23)
	v_cvt_pk_f16_f32 v4, v44, v45
	v_cvt_pk_f16_f32 v5, v46, v47
	ds_write_b64 v111, v[4:5] offset:2176
	global_load_dwordx4 v[44:47], v2, s[54:55] offset:1536 nt
	s_waitcnt vmcnt(23)
	v_cvt_pk_f16_f32 v4, v48, v49
	v_cvt_pk_f16_f32 v5, v50, v51
	ds_write_b64 v111, v[4:5] offset:4352
	global_load_dwordx4 v[48:51], v2, s[56:57] offset:1536 nt
	s_waitcnt vmcnt(23)
	v_cvt_pk_f16_f32 v4, v52, v53
	v_cvt_pk_f16_f32 v5, v54, v55
	ds_write_b64 v111, v[4:5] offset:6528
	global_load_dwordx4 v[52:55], v2, s[58:59] offset:1536 nt
	s_waitcnt vmcnt(23)
	v_cvt_pk_f16_f32 v4, v56, v57
	v_cvt_pk_f16_f32 v5, v58, v59
	ds_write_b64 v111, v[4:5] offset:8704
	global_load_dwordx4 v[56:59], v2, s[60:61] offset:1536 nt
	s_waitcnt vmcnt(23)
	v_cvt_pk_f16_f32 v4, v60, v61
	v_cvt_pk_f16_f32 v5, v62, v63
	ds_write_b64 v111, v[4:5] offset:10880
	global_load_dwordx4 v[60:63], v2, s[62:63] offset:1536 nt
	s_waitcnt vmcnt(23)
	v_cvt_pk_f16_f32 v4, v64, v65
	v_cvt_pk_f16_f32 v5, v66, v67
	ds_write_b64 v111, v[4:5] offset:13056
	global_load_dwordx4 v[64:67], v2, s[64:65] offset:1536 nt
	s_waitcnt vmcnt(23)
	v_cvt_pk_f16_f32 v4, v68, v69
	v_cvt_pk_f16_f32 v5, v70, v71
	ds_write_b64 v111, v[4:5] offset:15232
	global_load_dwordx4 v[68:71], v2, s[66:67] offset:1536 nt
	s_waitcnt lgkmcnt(0)
	s_barrier
	s_waitcnt vmcnt(23)
	v_cvt_pk_f16_f32 v4, v72, v73
	v_cvt_pk_f16_f32 v5, v74, v75
	ds_write_b64 v112, v[4:5]
	global_load_dwordx4 v[72:75], v2, s[52:53] offset:2048 nt
	s_waitcnt vmcnt(23)
	v_cvt_pk_f16_f32 v4, v76, v77
	v_cvt_pk_f16_f32 v5, v78, v79
	ds_write_b64 v112, v[4:5] offset:2176
	global_load_dwordx4 v[76:79], v2, s[54:55] offset:2048 nt
	s_waitcnt vmcnt(23)
	v_cvt_pk_f16_f32 v4, v80, v81
	v_cvt_pk_f16_f32 v5, v82, v83
	ds_write_b64 v112, v[4:5] offset:4352
	global_load_dwordx4 v[80:83], v2, s[56:57] offset:2048 nt
	s_waitcnt vmcnt(23)
	v_cvt_pk_f16_f32 v4, v84, v85
	v_cvt_pk_f16_f32 v5, v86, v87
	ds_write_b64 v112, v[4:5] offset:6528
	global_load_dwordx4 v[84:87], v2, s[58:59] offset:2048 nt
	s_waitcnt vmcnt(23)
	v_cvt_pk_f16_f32 v4, v88, v89
	v_cvt_pk_f16_f32 v5, v90, v91
	ds_write_b64 v112, v[4:5] offset:8704
	global_load_dwordx4 v[88:91], v2, s[60:61] offset:2048 nt
	s_waitcnt vmcnt(23)
	v_cvt_pk_f16_f32 v4, v92, v93
	v_cvt_pk_f16_f32 v5, v94, v95
	ds_write_b64 v112, v[4:5] offset:10880
	global_load_dwordx4 v[92:95], v2, s[62:63] offset:2048 nt
	s_waitcnt vmcnt(23)
	v_cvt_pk_f16_f32 v4, v96, v97
	v_cvt_pk_f16_f32 v5, v98, v99
	ds_write_b64 v112, v[4:5] offset:13056
	global_load_dwordx4 v[96:99], v2, s[64:65] offset:2048 nt
	s_waitcnt vmcnt(23)
	v_cvt_pk_f16_f32 v4, v100, v101
	v_cvt_pk_f16_f32 v5, v102, v103
	ds_write_b64 v112, v[4:5] offset:15232
	global_load_dwordx4 v[100:103], v2, s[66:67] offset:2048 nt
	s_waitcnt lgkmcnt(0)
	s_barrier
	s_waitcnt vmcnt(23)
	v_cvt_pk_f16_f32 v4, v8, v9
	v_cvt_pk_f16_f32 v5, v10, v11
	ds_write_b64 v110, v[4:5]
	global_load_dwordx4 v[8:11], v2, s[52:53] offset:2560 nt
	s_waitcnt vmcnt(23)
	v_cvt_pk_f16_f32 v4, v12, v13
	v_cvt_pk_f16_f32 v5, v14, v15
	ds_write_b64 v110, v[4:5] offset:2176
	global_load_dwordx4 v[12:15], v2, s[54:55] offset:2560 nt
	s_waitcnt vmcnt(23)
	v_cvt_pk_f16_f32 v4, v16, v17
	v_cvt_pk_f16_f32 v5, v18, v19
	ds_write_b64 v110, v[4:5] offset:4352
	global_load_dwordx4 v[16:19], v2, s[56:57] offset:2560 nt
	s_waitcnt vmcnt(23)
	v_cvt_pk_f16_f32 v4, v20, v21
	v_cvt_pk_f16_f32 v5, v22, v23
	ds_write_b64 v110, v[4:5] offset:6528
	global_load_dwordx4 v[20:23], v2, s[58:59] offset:2560 nt
	s_waitcnt vmcnt(23)
	v_cvt_pk_f16_f32 v4, v24, v25
	v_cvt_pk_f16_f32 v5, v26, v27
	ds_write_b64 v110, v[4:5] offset:8704
	global_load_dwordx4 v[24:27], v2, s[60:61] offset:2560 nt
	s_waitcnt vmcnt(23)
	v_cvt_pk_f16_f32 v4, v28, v29
	v_cvt_pk_f16_f32 v5, v30, v31
	ds_write_b64 v110, v[4:5] offset:10880
	global_load_dwordx4 v[28:31], v2, s[62:63] offset:2560 nt
	s_waitcnt vmcnt(23)
	v_cvt_pk_f16_f32 v4, v32, v33
	v_cvt_pk_f16_f32 v5, v34, v35
	ds_write_b64 v110, v[4:5] offset:13056
	global_load_dwordx4 v[32:35], v2, s[64:65] offset:2560 nt
	s_waitcnt vmcnt(23)
	v_cvt_pk_f16_f32 v4, v36, v37
	v_cvt_pk_f16_f32 v5, v38, v39
	ds_write_b64 v110, v[4:5] offset:15232
	global_load_dwordx4 v[36:39], v2, s[66:67] offset:2560 nt
	s_waitcnt lgkmcnt(0)
	s_barrier
	s_waitcnt vmcnt(23)
	v_cvt_pk_f16_f32 v4, v40, v41
	v_cvt_pk_f16_f32 v5, v42, v43
	ds_write_b64 v111, v[4:5]
	global_load_dwordx4 v[40:43], v2, s[52:53] offset:3072 nt
	s_waitcnt vmcnt(23)
	v_cvt_pk_f16_f32 v4, v44, v45
	v_cvt_pk_f16_f32 v5, v46, v47
	ds_write_b64 v111, v[4:5] offset:2176
	global_load_dwordx4 v[44:47], v2, s[54:55] offset:3072 nt
	s_waitcnt vmcnt(23)
	v_cvt_pk_f16_f32 v4, v48, v49
	v_cvt_pk_f16_f32 v5, v50, v51
	ds_write_b64 v111, v[4:5] offset:4352
	global_load_dwordx4 v[48:51], v2, s[56:57] offset:3072 nt
	s_waitcnt vmcnt(23)
	v_cvt_pk_f16_f32 v4, v52, v53
	v_cvt_pk_f16_f32 v5, v54, v55
	ds_write_b64 v111, v[4:5] offset:6528
	global_load_dwordx4 v[52:55], v2, s[58:59] offset:3072 nt
	s_waitcnt vmcnt(23)
	v_cvt_pk_f16_f32 v4, v56, v57
	v_cvt_pk_f16_f32 v5, v58, v59
	ds_write_b64 v111, v[4:5] offset:8704
	global_load_dwordx4 v[56:59], v2, s[60:61] offset:3072 nt
	s_waitcnt vmcnt(23)
	v_cvt_pk_f16_f32 v4, v60, v61
	v_cvt_pk_f16_f32 v5, v62, v63
	ds_write_b64 v111, v[4:5] offset:10880
	global_load_dwordx4 v[60:63], v2, s[62:63] offset:3072 nt
	s_waitcnt vmcnt(23)
	v_cvt_pk_f16_f32 v4, v64, v65
	v_cvt_pk_f16_f32 v5, v66, v67
	ds_write_b64 v111, v[4:5] offset:13056
	global_load_dwordx4 v[64:67], v2, s[64:65] offset:3072 nt
	s_waitcnt vmcnt(23)
	v_cvt_pk_f16_f32 v4, v68, v69
	v_cvt_pk_f16_f32 v5, v70, v71
	ds_write_b64 v111, v[4:5] offset:15232
	global_load_dwordx4 v[68:71], v2, s[66:67] offset:3072 nt
	s_waitcnt lgkmcnt(0)
	s_barrier
	s_waitcnt vmcnt(23)
	v_cvt_pk_f16_f32 v4, v72, v73
	v_cvt_pk_f16_f32 v5, v74, v75
	ds_write_b64 v112, v[4:5]
	v_mov_b32_e32 v72, 0
	v_mov_b32_e32 v73, 0
	v_mov_b32_e32 v74, 0
	v_mov_b32_e32 v75, 0
	s_mov_b64 s[70:71], exec
	s_mov_b64 exec, s[68:69]
	global_load_dwordx4 v[72:75], v2, s[52:53] offset:3584 nt
	s_mov_b64 exec, s[70:71]
	s_waitcnt vmcnt(23)
	v_cvt_pk_f16_f32 v4, v76, v77
	v_cvt_pk_f16_f32 v5, v78, v79
	ds_write_b64 v112, v[4:5] offset:2176
	v_mov_b32_e32 v76, 0
	v_mov_b32_e32 v77, 0
	v_mov_b32_e32 v78, 0
	v_mov_b32_e32 v79, 0
	s_mov_b64 s[70:71], exec
	s_mov_b64 exec, s[68:69]
	global_load_dwordx4 v[76:79], v2, s[54:55] offset:3584 nt
	s_mov_b64 exec, s[70:71]
	s_waitcnt vmcnt(23)
	v_cvt_pk_f16_f32 v4, v80, v81
	v_cvt_pk_f16_f32 v5, v82, v83
	ds_write_b64 v112, v[4:5] offset:4352
	v_mov_b32_e32 v80, 0
	v_mov_b32_e32 v81, 0
	v_mov_b32_e32 v82, 0
	v_mov_b32_e32 v83, 0
	s_mov_b64 s[70:71], exec
	s_mov_b64 exec, s[68:69]
	global_load_dwordx4 v[80:83], v2, s[56:57] offset:3584 nt
	s_mov_b64 exec, s[70:71]
	s_waitcnt vmcnt(23)
	v_cvt_pk_f16_f32 v4, v84, v85
	v_cvt_pk_f16_f32 v5, v86, v87
	ds_write_b64 v112, v[4:5] offset:6528
	v_mov_b32_e32 v84, 0
	v_mov_b32_e32 v85, 0
	v_mov_b32_e32 v86, 0
	v_mov_b32_e32 v87, 0
	s_mov_b64 s[70:71], exec
	s_mov_b64 exec, s[68:69]
	global_load_dwordx4 v[84:87], v2, s[58:59] offset:3584 nt
	s_mov_b64 exec, s[70:71]
	s_waitcnt vmcnt(23)
	v_cvt_pk_f16_f32 v4, v88, v89
	v_cvt_pk_f16_f32 v5, v90, v91
	ds_write_b64 v112, v[4:5] offset:8704
	v_mov_b32_e32 v88, 0
	v_mov_b32_e32 v89, 0
	v_mov_b32_e32 v90, 0
	v_mov_b32_e32 v91, 0
	s_mov_b64 s[70:71], exec
	s_mov_b64 exec, s[68:69]
	global_load_dwordx4 v[88:91], v2, s[60:61] offset:3584 nt
	s_mov_b64 exec, s[70:71]
	s_waitcnt vmcnt(23)
	v_cvt_pk_f16_f32 v4, v92, v93
	v_cvt_pk_f16_f32 v5, v94, v95
	ds_write_b64 v112, v[4:5] offset:10880
	v_mov_b32_e32 v92, 0
	v_mov_b32_e32 v93, 0
	v_mov_b32_e32 v94, 0
	v_mov_b32_e32 v95, 0
	s_mov_b64 s[70:71], exec
	s_mov_b64 exec, s[68:69]
	global_load_dwordx4 v[92:95], v2, s[62:63] offset:3584 nt
	s_mov_b64 exec, s[70:71]
	s_waitcnt vmcnt(23)
	v_cvt_pk_f16_f32 v4, v96, v97
	v_cvt_pk_f16_f32 v5, v98, v99
	ds_write_b64 v112, v[4:5] offset:13056
	v_mov_b32_e32 v96, 0
	v_mov_b32_e32 v97, 0
	v_mov_b32_e32 v98, 0
	v_mov_b32_e32 v99, 0
	s_mov_b64 s[70:71], exec
	s_mov_b64 exec, s[68:69]
	global_load_dwordx4 v[96:99], v2, s[64:65] offset:3584 nt
	s_mov_b64 exec, s[70:71]
	s_waitcnt vmcnt(23)
	v_cvt_pk_f16_f32 v4, v100, v101
	v_cvt_pk_f16_f32 v5, v102, v103
	ds_write_b64 v112, v[4:5] offset:15232
	v_mov_b32_e32 v100, 0
	v_mov_b32_e32 v101, 0
	v_mov_b32_e32 v102, 0
	v_mov_b32_e32 v103, 0
	s_mov_b64 s[70:71], exec
	s_mov_b64 exec, s[68:69]
	global_load_dwordx4 v[100:103], v2, s[66:67] offset:3584 nt
	s_mov_b64 exec, s[70:71]
	s_waitcnt lgkmcnt(0)
	s_barrier
	s_waitcnt vmcnt(23)
	v_cvt_pk_f16_f32 v4, v8, v9
	v_cvt_pk_f16_f32 v5, v10, v11
	ds_write_b64 v110, v[4:5]
	s_waitcnt vmcnt(22)
	v_cvt_pk_f16_f32 v4, v12, v13
	v_cvt_pk_f16_f32 v5, v14, v15
	ds_write_b64 v110, v[4:5] offset:2176
	s_waitcnt vmcnt(21)
	v_cvt_pk_f16_f32 v4, v16, v17
	v_cvt_pk_f16_f32 v5, v18, v19
	ds_write_b64 v110, v[4:5] offset:4352
	s_waitcnt vmcnt(20)
	v_cvt_pk_f16_f32 v4, v20, v21
	v_cvt_pk_f16_f32 v5, v22, v23
	ds_write_b64 v110, v[4:5] offset:6528
	s_waitcnt vmcnt(19)
	v_cvt_pk_f16_f32 v4, v24, v25
	v_cvt_pk_f16_f32 v5, v26, v27
	ds_write_b64 v110, v[4:5] offset:8704
	s_waitcnt vmcnt(18)
	v_cvt_pk_f16_f32 v4, v28, v29
	v_cvt_pk_f16_f32 v5, v30, v31
	ds_write_b64 v110, v[4:5] offset:10880
	s_waitcnt vmcnt(17)
	v_cvt_pk_f16_f32 v4, v32, v33
	v_cvt_pk_f16_f32 v5, v34, v35
	ds_write_b64 v110, v[4:5] offset:13056
	s_waitcnt vmcnt(16)
	v_cvt_pk_f16_f32 v4, v36, v37
	v_cvt_pk_f16_f32 v5, v38, v39
	ds_write_b64 v110, v[4:5] offset:15232
	s_waitcnt lgkmcnt(0)
	s_barrier
	s_waitcnt vmcnt(15)
	v_cvt_pk_f16_f32 v4, v40, v41
	v_cvt_pk_f16_f32 v5, v42, v43
	ds_write_b64 v111, v[4:5]
	s_waitcnt vmcnt(14)
	v_cvt_pk_f16_f32 v4, v44, v45
	v_cvt_pk_f16_f32 v5, v46, v47
	ds_write_b64 v111, v[4:5] offset:2176
	s_waitcnt vmcnt(13)
	v_cvt_pk_f16_f32 v4, v48, v49
	v_cvt_pk_f16_f32 v5, v50, v51
	ds_write_b64 v111, v[4:5] offset:4352
	s_waitcnt vmcnt(12)
	v_cvt_pk_f16_f32 v4, v52, v53
	v_cvt_pk_f16_f32 v5, v54, v55
	ds_write_b64 v111, v[4:5] offset:6528
	s_waitcnt vmcnt(11)
	v_cvt_pk_f16_f32 v4, v56, v57
	v_cvt_pk_f16_f32 v5, v58, v59
	ds_write_b64 v111, v[4:5] offset:8704
	s_waitcnt vmcnt(10)
	v_cvt_pk_f16_f32 v4, v60, v61
	v_cvt_pk_f16_f32 v5, v62, v63
	ds_write_b64 v111, v[4:5] offset:10880
	s_waitcnt vmcnt(9)
	v_cvt_pk_f16_f32 v4, v64, v65
	v_cvt_pk_f16_f32 v5, v66, v67
	ds_write_b64 v111, v[4:5] offset:13056
	s_waitcnt vmcnt(8)
	v_cvt_pk_f16_f32 v4, v68, v69
	v_cvt_pk_f16_f32 v5, v70, v71
	ds_write_b64 v111, v[4:5] offset:15232
	s_waitcnt lgkmcnt(0)
	s_barrier
	s_waitcnt vmcnt(7)
	v_cvt_pk_f16_f32 v4, v72, v73
	v_cvt_pk_f16_f32 v5, v74, v75
	s_mov_b64 s[70:71], exec
	s_mov_b64 exec, s[78:79]
	ds_write_b64 v112, v[4:5]
	s_mov_b64 exec, s[70:71]
	s_waitcnt vmcnt(6)
	v_cvt_pk_f16_f32 v4, v76, v77
	v_cvt_pk_f16_f32 v5, v78, v79
	s_mov_b64 s[70:71], exec
	s_mov_b64 exec, s[78:79]
	ds_write_b64 v112, v[4:5] offset:2176
	s_mov_b64 exec, s[70:71]
	s_waitcnt vmcnt(5)
	v_cvt_pk_f16_f32 v4, v80, v81
	v_cvt_pk_f16_f32 v5, v82, v83
	s_mov_b64 s[70:71], exec
	s_mov_b64 exec, s[78:79]
	ds_write_b64 v112, v[4:5] offset:4352
	s_mov_b64 exec, s[70:71]
	s_waitcnt vmcnt(4)
	v_cvt_pk_f16_f32 v4, v84, v85
	v_cvt_pk_f16_f32 v5, v86, v87
	s_mov_b64 s[70:71], exec
	s_mov_b64 exec, s[78:79]
	ds_write_b64 v112, v[4:5] offset:6528
	s_mov_b64 exec, s[70:71]
	s_waitcnt vmcnt(3)
	v_cvt_pk_f16_f32 v4, v88, v89
	v_cvt_pk_f16_f32 v5, v90, v91
	s_mov_b64 s[70:71], exec
	s_mov_b64 exec, s[78:79]
	ds_write_b64 v112, v[4:5] offset:8704
	s_mov_b64 exec, s[70:71]
	s_waitcnt vmcnt(2)
	v_cvt_pk_f16_f32 v4, v92, v93
	v_cvt_pk_f16_f32 v5, v94, v95
	s_mov_b64 s[70:71], exec
	s_mov_b64 exec, s[78:79]
	ds_write_b64 v112, v[4:5] offset:10880
	s_mov_b64 exec, s[70:71]
	s_waitcnt vmcnt(1)
	v_cvt_pk_f16_f32 v4, v96, v97
	v_cvt_pk_f16_f32 v5, v98, v99
	s_mov_b64 s[70:71], exec
	s_mov_b64 exec, s[78:79]
	ds_write_b64 v112, v[4:5] offset:13056
	s_mov_b64 exec, s[70:71]
	s_waitcnt vmcnt(0)
	v_cvt_pk_f16_f32 v4, v100, v101
	v_cvt_pk_f16_f32 v5, v102, v103
	s_mov_b64 s[70:71], exec
	s_mov_b64 exec, s[78:79]
	ds_write_b64 v112, v[4:5] offset:15232
	s_mov_b64 exec, s[70:71]
	s_waitcnt lgkmcnt(0)
	s_barrier
	s_barrier
	s_barrier
	s_endpgm
